# baseline (speedup 1.0000x reference)
.LBB0_11:
	s_add_i32 s3, s29, 0x4000
	s_add_i32 s19, s62, 0x0
	s_mov_b32 m0, s3
	s_nop 0
	buffer_load_dwordx4 v222, s[12:15], s19 offen lds
	s_add_i32 s10, s29, 0x4400
	s_add_i32 s0, s62, 0x400
	s_mov_b32 m0, s10
	s_nop 0
	buffer_load_dwordx4 v223, s[12:15], s0 offen lds
	s_add_i32 s11, s29, 0x4800
	s_add_i32 s18, s62, 0x800
	s_mov_b32 m0, s11
	s_nop 0
	buffer_load_dwordx4 v222, s[12:15], s18 offen lds
	s_add_i32 s16, s29, 0x4c00
	s_add_i32 s0, s62, 0xc00
	s_mov_b32 m0, s16
	s_nop 0
	buffer_load_dwordx4 v223, s[12:15], s0 offen lds
	v_mfma_f32_32x32x16_bf16 v[48:63], a[192:195], a[128:131], 0
	v_mfma_f32_32x32x16_bf16 v[32:47], a[192:195], a[160:163], 0
	v_mfma_f32_32x32x16_bf16 v[0:15], a[224:227], a[128:131], 0
	v_mfma_f32_32x32x16_bf16 v[16:31], a[224:227], a[160:163], 0
	v_mfma_f32_32x32x16_bf16 v[48:63], a[196:199], a[132:135], v[48:63]
	v_mfma_f32_32x32x16_bf16 v[32:47], a[196:199], a[164:167], v[32:47]
	v_mfma_f32_32x32x16_bf16 v[0:15], a[228:231], a[132:135], v[0:15]
	v_mfma_f32_32x32x16_bf16 v[16:31], a[228:231], a[164:167], v[16:31]
	v_mfma_f32_32x32x16_bf16 v[48:63], a[200:203], a[136:139], v[48:63]
	v_mfma_f32_32x32x16_bf16 v[32:47], a[200:203], a[168:171], v[32:47]
	v_mfma_f32_32x32x16_bf16 v[0:15], a[232:235], a[136:139], v[0:15]
	v_mfma_f32_32x32x16_bf16 v[16:31], a[232:235], a[168:171], v[16:31]
	v_mfma_f32_32x32x16_bf16 v[48:63], a[204:207], a[140:143], v[48:63]
	v_mfma_f32_32x32x16_bf16 v[32:47], a[204:207], a[172:175], v[32:47]
	v_mfma_f32_32x32x16_bf16 v[0:15], a[236:239], a[140:143], v[0:15]
	v_mfma_f32_32x32x16_bf16 v[16:31], a[236:239], a[172:175], v[16:31]
	v_mfma_f32_32x32x16_bf16 v[48:63], a[208:211], a[144:147], v[48:63]
	s_mov_b32 s27, s29
	v_mfma_f32_32x32x16_bf16 v[32:47], a[208:211], a[176:179], v[32:47]
	s_add_i32 s0, s63, 0x0
	s_mov_b32 s30, s0
	v_mfma_f32_32x32x16_bf16 v[0:15], a[240:243], a[144:147], v[0:15]
	s_mov_b32 s31, s20
	v_mfma_f32_32x32x16_bf16 v[16:31], a[240:243], a[176:179], v[16:31]
	s_add_i32 s33, s63, 0x400
	v_mfma_f32_32x32x16_bf16 v[48:63], a[212:215], a[148:151], v[48:63]
	s_mov_b32 s34, s21
	v_mfma_f32_32x32x16_bf16 v[32:47], a[212:215], a[180:183], v[32:47]
	s_add_i32 s1, s63, 0x800
	s_mov_b32 s35, s1
	v_mfma_f32_32x32x16_bf16 v[0:15], a[244:247], a[148:151], v[0:15]
	s_mov_b32 s36, s22
	v_mfma_f32_32x32x16_bf16 v[16:31], a[244:247], a[180:183], v[16:31]
	s_add_i32 s37, s63, 0xc00
	v_mfma_f32_32x32x16_bf16 v[48:63], a[216:219], a[152:155], v[48:63]
	s_add_i32 s23, s29, 0xc000
	s_mov_b32 s38, s23
	v_mfma_f32_32x32x16_bf16 v[32:47], a[216:219], a[184:187], v[32:47]
	v_mfma_f32_32x32x16_bf16 v[0:15], a[248:251], a[152:155], v[0:15]
	s_add_i32 s24, s29, 0xc400
	s_mov_b32 s39, s24
	v_mfma_f32_32x32x16_bf16 v[16:31], a[248:251], a[184:187], v[16:31]
	s_add_i32 s40, s62, 0x80
	v_mfma_f32_32x32x16_bf16 v[48:63], a[220:223], a[156:159], v[48:63]
	s_add_i32 s25, s29, 0xc800
	s_mov_b32 s41, s25
	v_mfma_f32_32x32x16_bf16 v[32:47], a[220:223], a[188:191], v[32:47]
	v_mfma_f32_32x32x16_bf16 v[0:15], a[252:255], a[156:159], v[0:15]
	s_add_i32 s26, s29, 0xcc00
	s_mov_b32 s42, s26
	v_mfma_f32_32x32x16_bf16 v[16:31], a[252:255], a[188:191], v[16:31]
	s_add_i32 s43, s62, 0x880
	s_waitcnt vmcnt(0) lgkmcnt(0)
	s_barrier
	s_nop 0
	s_mov_b32 m0, s27
	s_nop 0
	buffer_load_dwordx4 v222, s[12:15], s30 offen lds
	s_mov_b32 m0, s31
	s_nop 0
	buffer_load_dwordx4 v223, s[12:15], s33 offen lds
	s_addk_i32 s17, 0x4000
	v_add_u32_e32 v217, s17, v64
	ds_read_b128 a[192:195], v217 offset:0
	s_mov_b32 m0, s34
	s_nop 0
	buffer_load_dwordx4 v222, s[12:15], s35 offen lds
	v_add_u32_e32 v199, s17, v65
	ds_read_b128 a[196:199], v199 offset:0
	s_mov_b32 m0, s36
	s_nop 0
	buffer_load_dwordx4 v223, s[12:15], s37 offen lds
	v_add_u32_e32 v198, s17, v66
	ds_read_b128 a[200:203], v198 offset:0
	s_mov_b32 m0, s38
	s_nop 0
	buffer_load_dwordx4 v196, s[4:7], s19 offen lds
	v_add_u32_e32 v197, s17, v67
	ds_read_b128 a[204:207], v197 offset:0
	s_mov_b32 m0, s39
	s_nop 0
	buffer_load_dwordx4 v196, s[4:7], s40 offen lds
	ds_read_b128 a[208:211], v217 offset:128
	s_mov_b32 m0, s41
	s_nop 0
	buffer_load_dwordx4 v196, s[4:7], s18 offen lds
	ds_read_b128 a[212:215], v199 offset:128
	s_mov_b32 m0, s42
	s_nop 0
	buffer_load_dwordx4 v196, s[4:7], s43 offen lds
	ds_read_b128 a[216:219], v198 offset:128
	ds_read_b128 a[220:223], v197 offset:128
	v_cvt_pk_bf16_f32 v248, v248, v249
	v_cvt_pk_bf16_f32 v249, v250, v251
	v_cvt_pk_bf16_f32 v250, v252, v253
	v_cvt_pk_bf16_f32 v251, v254, v255
	v_lshrrev_b32_e32 v252, 1, v208
	buffer_store_dwordx4 v[248:251], v252, s[12:15], s56 offen sc1
	v_mbcnt_lo_u32_b32 v253, -1, 0
	v_mbcnt_hi_u32_b32 v253, -1, v253
	v_lshlrev_b32_e32 v253, 4, v253
	v_add_u32_e32 v253, s84, v253
	ds_read_b128 v[248:251], v253
	ds_read_b128 v[252:255], v253 offset:1024
	v_max3_f32 v64, v48, v49, v0
	v_max3_f32 v65, v50, v51, v1
	v_max3_f32 v64, v64, v2, v3
	ds_read_b128 a[224:227], v217 offset:8192
	v_max3_f32 v64, v64, v52, v53
	v_max3_f32 v65, v65, v54, v55
	v_max3_f32 v64, v64, v4, v5
	v_max3_f32 v65, v65, v6, v7
	ds_read_b128 a[228:231], v199 offset:8192
	v_max3_f32 v64, v64, v56, v57
	v_max3_f32 v65, v65, v58, v59
	v_max3_f32 v64, v64, v8, v9
	v_max3_f32 v65, v65, v10, v11
	ds_read_b128 a[232:235], v198 offset:8192
	v_max3_f32 v64, v64, v60, v61
	v_max3_f32 v65, v65, v62, v63
	v_max3_f32 v64, v64, v12, v13
	v_max3_f32 v65, v65, v14, v15
	ds_read_b128 a[236:239], v197 offset:8192
	v_max3_f32 v66, v32, v33, v16
	v_max3_f32 v67, v34, v35, v17
	v_max3_f32 v66, v66, v18, v19
	ds_read_b128 a[240:243], v217 offset:8320
	v_max3_f32 v66, v66, v36, v37
	v_max3_f32 v67, v67, v38, v39
	v_max3_f32 v66, v66, v20, v21
	v_max3_f32 v67, v67, v22, v23
	ds_read_b128 a[244:247], v199 offset:8320
	v_max3_f32 v66, v66, v40, v41
	v_max3_f32 v67, v67, v42, v43
	v_max3_f32 v66, v66, v24, v25
	v_max3_f32 v67, v67, v26, v27
	ds_read_b128 a[248:251], v198 offset:8320
	v_max3_f32 v66, v66, v44, v45
	v_max3_f32 v67, v67, v46, v47
	v_max3_f32 v66, v66, v28, v29
	v_max3_f32 v67, v67, v30, v31
	ds_read_b128 a[252:255], v197 offset:8320
	s_waitcnt lgkmcnt(8)
	v_pk_add_f32 v[200:201], v[248:249], v[200:201]
	v_pk_add_f32 v[202:203], v[250:251], v[202:203]
	v_pk_add_f32 v[204:205], v[252:253], v[204:205]
	v_pk_add_f32 v[206:207], v[254:255], v[206:207]
	v_cvt_pk_bf16_f32 v248, v248, v249
	v_cvt_pk_bf16_f32 v249, v250, v251
	v_cvt_pk_bf16_f32 v250, v252, v253
	v_cvt_pk_bf16_f32 v251, v254, v255
	v_lshrrev_b32_e32 v252, 1, v208
	buffer_store_dwordx4 v[248:251], v252, s[4:7], s56 offen sc1
	s_add_i32 s56, s56, 0x1000
	s_nop 1
	global_load_dwordx4 v[248:251], v208, s[54:55] nt
	global_load_dwordx4 v[252:255], v208, s[54:55] offset:16 nt
	s_add_u32 s54, s54, 0x2000
	s_addc_u32 s55, s55, 0
	s_mov_b32 m0, s84
	s_nop 0
	buffer_load_dwordx4 v208, s[80:83], s86 offen lds
	s_mov_b32 m0, s85
	s_nop 0
	buffer_load_dwordx4 v208, s[80:83], s86 offen offset:16 lds
	s_add_i32 s86, s86, 0x2000
	v_max_f32_e32 v64, v64, v65
	v_mov_b32_e32 v65, v64
	s_nop 1
	v_permlane32_swap_b32_e32 v64, v65
	v_max_f32_e32 v214, v64, v65
	v_max_f32_e32 v64, v66, v67
	v_mov_b32_e32 v65, v64
	s_nop 1
	v_permlane32_swap_b32_e32 v64, v65
	v_max_f32_e32 v213, v64, v65
	v_sub_f32_e32 v64, v0, v214
	v_mbcnt_lo_u32_b32 v0, -1, 0
	v_mbcnt_hi_u32_b32 v0, -1, v0
	v_sub_f32_e32 v65, v1, v214
	v_xor_b32_e32 v1, 0x80000000, v214
	v_cmp_gt_u32_e32 vcc, 32, v0
	v_sub_f32_e32 v128, v2, v214
	v_sub_f32_e32 v129, v3, v214
	v_sub_f32_e32 v130, v4, v214
	v_sub_f32_e32 v131, v5, v214
	v_sub_f32_e32 v132, v6, v214
	v_sub_f32_e32 v133, v7, v214
	v_sub_f32_e32 v134, v8, v214
	v_sub_f32_e32 v135, v9, v214
	v_sub_f32_e32 v136, v10, v214
	v_sub_f32_e32 v137, v11, v214
	v_sub_f32_e32 v138, v12, v214
	v_sub_f32_e32 v139, v13, v214
	v_sub_f32_e32 v140, v14, v214
	v_sub_f32_e32 v141, v15, v214
	v_sub_f32_e32 v142, v16, v213
	v_mov_b32_e32 v211, 1.0
	v_sub_f32_e32 v143, v17, v213
	v_xor_b32_e32 v17, 0x80000000, v213
	v_cndmask_b32_e64 v0, 0, 1.0, vcc
	s_nop 1
	v_mfma_f32_32x32x2_f32 v[0:15], v0, v1, 0
	v_mbcnt_lo_u32_b32 v16, -1, 0
	v_mbcnt_hi_u32_b32 v16, -1, v16
	v_sub_f32_e32 v48, v48, v214
	v_sub_f32_e32 v49, v49, v214
	v_sub_f32_e32 v50, v50, v214
	v_sub_f32_e32 v51, v51, v214
	v_sub_f32_e32 v52, v52, v214
	v_sub_f32_e32 v53, v53, v214
	v_sub_f32_e32 v54, v54, v214
	v_sub_f32_e32 v55, v55, v214
	v_sub_f32_e32 v56, v56, v214
	v_sub_f32_e32 v57, v57, v214
	v_sub_f32_e32 v58, v58, v214
	v_sub_f32_e32 v59, v59, v214
	v_sub_f32_e32 v60, v60, v214
	v_sub_f32_e32 v61, v61, v214
	v_sub_f32_e32 v62, v62, v214
	v_sub_f32_e32 v63, v63, v214
	v_sub_f32_e32 v32, v32, v213
	v_sub_f32_e32 v33, v33, v213
	v_sub_f32_e32 v34, v34, v213
	v_cmp_gt_u32_e32 vcc, 32, v16
	v_sub_f32_e32 v35, v35, v213
	v_sub_f32_e32 v36, v36, v213
	v_sub_f32_e32 v37, v37, v213
	v_sub_f32_e32 v38, v38, v213
	v_sub_f32_e32 v39, v39, v213
	v_sub_f32_e32 v40, v40, v213
	v_sub_f32_e32 v41, v41, v213
	v_sub_f32_e32 v42, v42, v213
	v_sub_f32_e32 v43, v43, v213
	v_sub_f32_e32 v44, v44, v213
	v_sub_f32_e32 v45, v45, v213
	v_sub_f32_e32 v46, v46, v213
	v_sub_f32_e32 v47, v47, v213
	v_sub_f32_e32 v144, v18, v213
	v_sub_f32_e32 v145, v19, v213
	v_sub_f32_e32 v146, v20, v213
	v_sub_f32_e32 v147, v21, v213
	v_sub_f32_e32 v183, v22, v213
	v_sub_f32_e32 v194, v23, v213
	v_cndmask_b32_e64 v16, 0, 1.0, vcc
	v_sub_f32_e32 v195, v24, v213
	v_sub_f32_e32 v215, v25, v213
	v_sub_f32_e32 v216, v26, v213
	v_sub_f32_e32 v224, v27, v213
	v_sub_f32_e32 v225, v28, v213
	v_sub_f32_e32 v226, v29, v213
	v_sub_f32_e32 v229, v30, v213
	v_sub_f32_e32 v230, v31, v213
	v_mfma_f32_32x32x2_f32 v[16:31], v16, v17, 0
	v_exp_f32_e32 v112, v48
	v_exp_f32_e32 v113, v49
	v_exp_f32_e32 v114, v50
	v_exp_f32_e32 v115, v51
	v_mov_b32_e32 v193, 0
	v_add_f32_e32 v48, v193, v112
	v_add_f32_e32 v49, v193, v113
	v_exp_f32_e32 v116, v52
	v_exp_f32_e32 v117, v53
	v_exp_f32_e32 v118, v54
	v_add_f32_e32 v48, v48, v114
	v_add_f32_e32 v49, v49, v115
	v_exp_f32_e32 v119, v55
	v_exp_f32_e32 v120, v56
	v_add_f32_e32 v48, v48, v116
	v_add_f32_e32 v49, v49, v117
	v_add_f32_e32 v48, v48, v118
	v_exp_f32_e32 v121, v57
	v_exp_f32_e32 v122, v58
	v_exp_f32_e32 v123, v59
	v_add_f32_e32 v49, v49, v119
	v_add_f32_e32 v48, v48, v120
	v_exp_f32_e32 v124, v60
	v_exp_f32_e32 v125, v61
	v_add_f32_e32 v49, v49, v121
	v_add_f32_e32 v48, v48, v122
	v_add_f32_e32 v49, v49, v123
	v_exp_f32_e32 v126, v62
	v_exp_f32_e32 v127, v63
	v_exp_f32_e32 v96, v32
	v_add_f32_e32 v32, v48, v124
	v_add_f32_e32 v48, v49, v125
	v_exp_f32_e32 v97, v33
	v_exp_f32_e32 v98, v34
	v_add_f32_e32 v231, v32, v126
	v_add_f32_e32 v232, v48, v127
	v_add_f32_e32 v32, v193, v96
	v_exp_f32_e32 v99, v35
	v_exp_f32_e32 v100, v36
	v_exp_f32_e32 v101, v37
	v_add_f32_e32 v33, v193, v97
	v_add_f32_e32 v32, v32, v98
	v_exp_f32_e32 v102, v38
	v_exp_f32_e32 v103, v39
	v_add_f32_e32 v33, v33, v99
	v_add_f32_e32 v32, v32, v100
	v_add_f32_e32 v33, v33, v101
	v_exp_f32_e32 v104, v40
	v_exp_f32_e32 v105, v41
	v_exp_f32_e32 v106, v42
	v_add_f32_e32 v32, v32, v102
	v_add_f32_e32 v33, v33, v103
	v_exp_f32_e32 v107, v43
	v_exp_f32_e32 v108, v44
	v_add_f32_e32 v32, v32, v104
	v_add_f32_e32 v33, v33, v105
	v_add_f32_e32 v32, v32, v106
	v_exp_f32_e32 v109, v45
	v_exp_f32_e32 v110, v46
	v_exp_f32_e32 v111, v47
	v_add_f32_e32 v33, v33, v107
	v_add_f32_e32 v32, v32, v108
	s_waitcnt lgkmcnt(0)
	v_add_f32_e32 v33, v33, v109
	v_add_f32_e32 v233, v32, v110
	v_add_f32_e32 v234, v33, v111
	v_mfma_f32_32x32x16_bf16 v[80:95], a[192:195], a[128:131], v[0:15]
	ds_read_b64_tr_b16 v[160:161], v212 offset:0
	v_exp_f32_e32 v235, v64
	v_exp_f32_e32 v236, v65
	v_cvt_pk_bf16_f32 v152, v112, v113
	v_mfma_f32_32x32x16_bf16 v[64:79], a[192:195], a[160:163], v[16:31]
	ds_read_b64_tr_b16 v[162:163], v212 offset:0x800
	v_exp_f32_e32 v237, v128
	v_exp_f32_e32 v238, v129
	v_cvt_pk_bf16_f32 v153, v114, v115
	v_mfma_f32_32x32x16_bf16 v[48:63], a[224:227], a[128:131], v[0:15]
	v_exp_f32_e32 v115, v130
	ds_read_b64_tr_b16 v[172:173], v212 offset:0x200
	v_exp_f32_e32 v239, v131
	v_cvt_pk_bf16_f32 v154, v116, v117
	v_mfma_f32_32x32x16_bf16 v[32:47], a[224:227], a[160:163], v[16:31]
	ds_read_b64_tr_b16 v[174:175], v212 offset:0xa00
	ds_read_b64_tr_b16 v[168:169], v212 offset:0x400
	v_exp_f32_e32 v240, v132
	v_exp_f32_e32 v241, v133
	v_cvt_pk_bf16_f32 v155, v118, v119
	v_mfma_f32_32x32x16_bf16 v[80:95], a[196:199], a[132:135], v[80:95]
	v_exp_f32_e32 v185, v134
	v_exp_f32_e32 v186, v135
	ds_read_b64_tr_b16 v[170:171], v212 offset:0xc00
	v_cvt_pk_bf16_f32 v128, v120, v121
	v_mfma_f32_32x32x16_bf16 v[64:79], a[196:199], a[164:167], v[64:79]
	v_exp_f32_e32 v187, v136
	v_exp_f32_e32 v188, v137
	ds_read_b64_tr_b16 v[176:177], v212 offset:0x600
	v_cvt_pk_bf16_f32 v129, v122, v123
	v_mfma_f32_32x32x16_bf16 v[48:63], a[228:231], a[132:135], v[48:63]
	v_exp_f32_e32 v189, v138
	v_exp_f32_e32 v190, v139
	ds_read_b64_tr_b16 v[178:179], v212 offset:0xe00
	v_cvt_pk_bf16_f32 v130, v124, v125
	v_mfma_f32_32x32x16_bf16 v[32:47], a[228:231], a[164:167], v[32:47]
	ds_read_b64_tr_b16 v[164:165], v212 offset:0x1000
	v_exp_f32_e32 v191, v140
	v_exp_f32_e32 v192, v141
	ds_read_b64_tr_b16 v[166:167], v212 offset:0x1800
	v_cvt_pk_bf16_f32 v131, v126, v127
	v_mfma_f32_32x32x16_bf16 v[80:95], a[200:203], a[136:139], v[80:95]
	v_exp_f32_e32 v141, v142
	v_exp_f32_e32 v142, v143
	ds_read_b64_tr_b16 v[156:157], v212 offset:0x1200
	v_cvt_pk_bf16_f32 v180, v96, v97
	v_mfma_f32_32x32x16_bf16 v[64:79], a[200:203], a[168:171], v[64:79]
	v_exp_f32_e32 v143, v144
	ds_read_b64_tr_b16 v[158:159], v212 offset:0x1a00
	v_exp_f32_e32 v242, v145
	v_cvt_pk_bf16_f32 v181, v98, v99
	v_mfma_f32_32x32x16_bf16 v[48:63], a[232:235], a[136:139], v[48:63]
	ds_read_b64_tr_b16 v[148:149], v212 offset:0x1400
	v_exp_f32_e32 v243, v146
	v_exp_f32_e32 v244, v147
	v_cvt_pk_bf16_f32 v182, v100, v101
	v_mfma_f32_32x32x16_bf16 v[32:47], a[232:235], a[168:171], v[32:47]
	ds_read_b64_tr_b16 v[150:151], v212 offset:0x1c00
	ds_read_b64_tr_b16 v[136:137], v212 offset:0x1600
	v_exp_f32_e32 v245, v183
	v_exp_f32_e32 v246, v194
	v_cvt_pk_bf16_f32 v183, v102, v103
	v_mfma_f32_32x32x16_bf16 v[80:95], a[204:207], a[140:143], v[80:95]
	v_exp_f32_e32 v194, v195
	v_exp_f32_e32 v195, v215
	ds_read_b64_tr_b16 v[138:139], v212 offset:0x1e00
	v_cvt_pk_bf16_f32 v144, v104, v105
	v_mfma_f32_32x32x16_bf16 v[64:79], a[204:207], a[172:175], v[64:79]
	v_exp_f32_e32 v215, v216
	v_exp_f32_e32 v224, v224
	ds_read_b64_tr_b16 v[132:133], v212 offset:0x2000
	v_cvt_pk_bf16_f32 v145, v106, v107
	v_mfma_f32_32x32x16_bf16 v[48:63], a[236:239], a[140:143], v[48:63]
	v_exp_f32_e32 v227, v225
	v_exp_f32_e32 v228, v226
	ds_read_b64_tr_b16 v[134:135], v212 offset:0x2800
	v_cvt_pk_bf16_f32 v146, v108, v109
	v_mfma_f32_32x32x16_bf16 v[32:47], a[236:239], a[172:175], v[32:47]
	ds_read_b64_tr_b16 v[124:125], v212 offset:0x2200
	v_exp_f32_e32 v229, v229
	v_exp_f32_e32 v230, v230
	ds_read_b64_tr_b16 v[126:127], v212 offset:0x2a00
	v_cvt_pk_bf16_f32 v147, v110, v111
	s_mov_b32 s27, s3
	v_mfma_f32_32x32x16_bf16 v[80:95], a[208:211], a[144:147], v[80:95]
	ds_read_b64_tr_b16 v[120:121], v212 offset:0x2400
	v_cvt_pk_bf16_f32 v112, v235, v236
	v_add_f32_e32 v96, v231, v235
	v_add_f32_e32 v97, v232, v236
	s_add_i32 s30, s87, 0x0
	v_mfma_f32_32x32x16_bf16 v[64:79], a[208:211], a[176:179], v[64:79]
	ds_read_b64_tr_b16 v[122:123], v212 offset:0x2c00
	v_cvt_pk_bf16_f32 v113, v237, v238
	v_add_f32_e32 v96, v96, v237
	v_add_f32_e32 v97, v97, v238
	s_mov_b32 s31, s10
	v_mfma_f32_32x32x16_bf16 v[48:63], a[240:243], a[144:147], v[48:63]
	ds_read_b64_tr_b16 v[116:117], v212 offset:0x2600
	v_cvt_pk_bf16_f32 v114, v115, v239
	v_add_f32_e32 v96, v96, v115
	v_add_f32_e32 v97, v97, v239
	s_add_i32 s33, s87, 0x400
	v_mfma_f32_32x32x16_bf16 v[32:47], a[240:243], a[176:179], v[32:47]
	ds_read_b64_tr_b16 v[118:119], v212 offset:0x2e00
	ds_read_b64_tr_b16 v[104:105], v212 offset:0x3000
	v_cvt_pk_bf16_f32 v115, v240, v241
	v_add_f32_e32 v96, v96, v240
	v_add_f32_e32 v97, v97, v241
	s_mov_b32 s34, s11
	v_mfma_f32_32x32x16_bf16 v[80:95], a[212:215], a[148:151], v[80:95]
	ds_read_b64_tr_b16 v[106:107], v212 offset:0x3800
	v_add_f32_e32 v96, v96, v185
	v_add_f32_e32 v97, v97, v186
	s_add_i32 s35, s87, 0x800
	v_mfma_f32_32x32x16_bf16 v[64:79], a[212:215], a[180:183], v[64:79]
	ds_read_b64_tr_b16 v[108:109], v212 offset:0x3200
	v_add_f32_e32 v96, v96, v187
	v_add_f32_e32 v97, v97, v188
	s_mov_b32 s36, s16
	v_mfma_f32_32x32x16_bf16 v[48:63], a[244:247], a[148:151], v[48:63]
	ds_read_b64_tr_b16 v[110:111], v212 offset:0x3a00
	v_add_f32_e32 v96, v96, v189
	v_add_f32_e32 v97, v97, v190
	s_add_i32 s37, s87, 0xc00
	v_mfma_f32_32x32x16_bf16 v[32:47], a[244:247], a[180:183], v[32:47]
	ds_read_b64_tr_b16 v[100:101], v212 offset:0x3400
	ds_read_b64_tr_b16 v[102:103], v212 offset:0x3c00
	v_add_f32_e32 v216, v96, v191
	v_add_f32_e32 v225, v97, v192
	s_mov_b32 s38, s2
	v_mfma_f32_32x32x16_bf16 v[80:95], a[216:219], a[152:155], v[80:95]
	ds_read_b64_tr_b16 v[96:97], v212 offset:0x3600
	v_cvt_pk_bf16_f32 v140, v141, v142
	v_add_f32_e32 v226, v233, v141
	v_add_f32_e32 v142, v234, v142
	v_mfma_f32_32x32x16_bf16 v[64:79], a[216:219], a[184:187], v[64:79]
	ds_read_b64_tr_b16 v[98:99], v212 offset:0x3e00
	v_cvt_pk_bf16_f32 v141, v143, v242
	v_add_f32_e32 v143, v226, v143
	v_add_f32_e32 v226, v142, v242
	v_mfma_f32_32x32x16_bf16 v[48:63], a[248:251], a[152:155], v[48:63]
	s_add_i32 s17, s29, 0x8400
	s_mov_b32 s39, s17
	v_cvt_pk_bf16_f32 v142, v243, v244
	v_add_f32_e32 v231, v143, v243
	v_add_f32_e32 v226, v226, v244
	v_mfma_f32_32x32x16_bf16 v[32:47], a[248:251], a[184:187], v[32:47]
	s_add_i32 s40, s63, 0x80
	v_cvt_pk_bf16_f32 v143, v245, v246
	v_add_f32_e32 v231, v231, v245
	v_add_f32_e32 v226, v226, v246
	v_mfma_f32_32x32x16_bf16 v[80:95], a[220:223], a[156:159], v[80:95]
	s_add_i32 s18, s29, 0x8800
	s_mov_b32 s41, s18
	v_add_f32_e32 v231, v231, v194
	v_add_f32_e32 v226, v226, v195
	v_mfma_f32_32x32x16_bf16 v[64:79], a[220:223], a[188:191], v[64:79]
	v_add_f32_e32 v231, v231, v215
	v_add_f32_e32 v226, v226, v224
	v_mfma_f32_32x32x16_bf16 v[48:63], a[252:255], a[156:159], v[48:63]
	s_add_i32 s19, s29, 0x8c00
	s_mov_b32 s42, s19
	v_add_f32_e32 v231, v231, v227
	v_add_f32_e32 v226, v226, v228
	v_mfma_f32_32x32x16_bf16 v[32:47], a[252:255], a[188:191], v[32:47]
	s_add_i32 s43, s63, 0x880
	v_add_f32_e32 v231, v231, v229
	v_add_f32_e32 v226, v226, v230
	v_add_f32_e32 v216, v216, v225
	s_waitcnt vmcnt(0) lgkmcnt(0)
	s_barrier
	s_mov_b32 m0, s27
	v_mfma_f32_32x32x16_bf16 a[0:15], v[160:163], v[152:155], 0
	v_mov_b32_e32 v225, v216
	buffer_load_dwordx4 v222, s[12:15], s30 offen lds
	s_mov_b32 m0, s31
	v_mfma_f32_32x32x16_bf16 a[16:31], v[160:163], v[180:183], 0
	v_permlane32_swap_b32_e32 v216, v225
	v_add_f32_e32 v216, v216, v225
	buffer_load_dwordx4 v223, s[12:15], s33 offen lds
	ds_read_b128 a[192:195], v218 offset:0
	s_mov_b32 m0, s34
	v_mfma_f32_32x32x16_bf16 a[32:47], v[172:175], v[152:155], 0
	v_add_f32_e32 v225, v193, v216
	v_add_f32_e32 v216, v231, v226
	v_mov_b32_e32 v226, v216
	buffer_load_dwordx4 v222, s[12:15], s35 offen lds
	ds_read_b128 a[196:199], v219 offset:0
	s_mov_b32 m0, s36
	v_mfma_f32_32x32x16_bf16 a[48:63], v[172:175], v[180:183], 0
	v_permlane32_swap_b32_e32 v216, v226
	v_add_f32_e32 v216, v216, v226
	buffer_load_dwordx4 v223, s[12:15], s37 offen lds
	ds_read_b128 a[200:203], v220 offset:0
	s_mov_b32 m0, s38
	v_mfma_f32_32x32x16_bf16 a[64:79], v[168:171], v[152:155], 0
	v_add_f32_e32 v226, v193, v216
	buffer_load_dwordx4 v196, s[4:7], s0 offen lds
	ds_read_b128 a[204:207], v221 offset:0
	s_mov_b32 m0, s39
	v_mfma_f32_32x32x16_bf16 a[80:95], v[168:171], v[180:183], 0
	buffer_load_dwordx4 v196, s[4:7], s40 offen lds
	ds_read_b128 a[208:211], v218 offset:128
	s_mov_b32 m0, s41
	v_mfma_f32_32x32x16_bf16 a[96:111], v[176:179], v[152:155], 0
	buffer_load_dwordx4 v196, s[4:7], s1 offen lds
	ds_read_b128 a[212:215], v219 offset:128
	s_mov_b32 m0, s42
	v_mfma_f32_32x32x16_bf16 a[112:127], v[176:179], v[180:183], 0
	buffer_load_dwordx4 v196, s[4:7], s43 offen lds
	ds_read_b128 a[216:219], v220 offset:128
	v_mfma_f32_32x32x16_bf16 a[0:15], v[164:167], v[128:131], a[0:15]
	ds_read_b128 a[220:223], v221 offset:128
	v_cvt_pk_bf16_f32 v248, v248, v249
	v_cvt_pk_bf16_f32 v249, v250, v251
	v_cvt_pk_bf16_f32 v250, v252, v253
	v_cvt_pk_bf16_f32 v251, v254, v255
	v_lshrrev_b32_e32 v252, 1, v208
	buffer_store_dwordx4 v[248:251], v252, s[12:15], s56 offen sc1
	v_mbcnt_lo_u32_b32 v253, -1, 0
	v_mbcnt_hi_u32_b32 v253, -1, v253
	v_lshlrev_b32_e32 v253, 4, v253
	v_add_u32_e32 v253, s84, v253
	ds_read_b128 v[248:251], v253
	ds_read_b128 v[252:255], v253 offset:1024
	v_max3_f32 v152, v80, v81, v48
	v_max3_f32 v153, v82, v83, v49
	v_max3_f32 v152, v152, v50, v51
	v_mfma_f32_32x32x16_bf16 a[16:31], v[164:167], v[144:147], a[16:31]
	ds_read_b128 a[224:227], v218 offset:8192
	v_max3_f32 v152, v152, v84, v85
	v_max3_f32 v153, v153, v86, v87
	v_max3_f32 v152, v152, v52, v53
	v_max3_f32 v153, v153, v54, v55
	v_mfma_f32_32x32x16_bf16 a[32:47], v[156:159], v[128:131], a[32:47]
	ds_read_b128 a[228:231], v219 offset:8192
	v_max3_f32 v152, v152, v88, v89
	v_max3_f32 v153, v153, v90, v91
	v_max3_f32 v152, v152, v56, v57
	v_max3_f32 v153, v153, v58, v59
	v_mfma_f32_32x32x16_bf16 a[48:63], v[156:159], v[144:147], a[48:63]
	ds_read_b128 a[232:235], v220 offset:8192
	v_max3_f32 v152, v152, v92, v93
	v_max3_f32 v153, v153, v94, v95
	v_max3_f32 v152, v152, v60, v61
	v_max3_f32 v153, v153, v62, v63
	v_mfma_f32_32x32x16_bf16 a[64:79], v[148:151], v[128:131], a[64:79]
	ds_read_b128 a[236:239], v221 offset:8192
	v_max3_f32 v154, v64, v65, v32
	v_max3_f32 v155, v66, v67, v33
	v_max3_f32 v154, v154, v34, v35
	v_mfma_f32_32x32x16_bf16 a[80:95], v[148:151], v[144:147], a[80:95]
	ds_read_b128 a[240:243], v218 offset:8320
	v_max3_f32 v148, v154, v68, v69
	v_max3_f32 v149, v155, v70, v71
	v_max3_f32 v148, v148, v36, v37
	v_max3_f32 v149, v149, v38, v39
	v_mfma_f32_32x32x16_bf16 a[96:111], v[136:139], v[128:131], a[96:111]
	ds_read_b128 a[244:247], v219 offset:8320
	v_max3_f32 v128, v148, v72, v73
	v_max3_f32 v129, v149, v74, v75
	v_max3_f32 v128, v128, v40, v41
	v_max3_f32 v129, v129, v42, v43
	v_mfma_f32_32x32x16_bf16 a[112:127], v[136:139], v[144:147], a[112:127]
	ds_read_b128 a[248:251], v220 offset:8320
	v_max3_f32 v128, v128, v76, v77
	v_max3_f32 v129, v129, v78, v79
	v_max3_f32 v128, v128, v44, v45
	v_max3_f32 v130, v129, v46, v47
	v_mfma_f32_32x32x16_bf16 a[0:15], v[132:135], v[112:115], a[0:15]
	ds_read_b128 a[252:255], v221 offset:8320
	s_waitcnt lgkmcnt(8)
	v_pk_add_f32 v[200:201], v[248:249], v[200:201]
	v_pk_add_f32 v[202:203], v[250:251], v[202:203]
	v_pk_add_f32 v[204:205], v[252:253], v[204:205]
	v_pk_add_f32 v[206:207], v[254:255], v[206:207]
	v_cvt_pk_bf16_f32 v248, v248, v249
	v_cvt_pk_bf16_f32 v249, v250, v251
	v_cvt_pk_bf16_f32 v250, v252, v253
	v_cvt_pk_bf16_f32 v251, v254, v255
	v_lshrrev_b32_e32 v252, 1, v208
	buffer_store_dwordx4 v[248:251], v252, s[4:7], s56 offen sc1
	s_add_i32 s56, s56, 0x1000
	s_nop 1
	global_load_dwordx4 v[248:251], v208, s[54:55] nt
	global_load_dwordx4 v[252:255], v208, s[54:55] offset:16 nt
	s_add_u32 s54, s54, 0x2000
	s_addc_u32 s55, s55, 0
	s_mov_b32 m0, s84
	s_nop 0
	buffer_load_dwordx4 v208, s[80:83], s86 offen lds
	s_mov_b32 m0, s85
	s_nop 0
	buffer_load_dwordx4 v208, s[80:83], s86 offen offset:16 lds
	s_add_i32 s86, s86, 0x2000
	v_max_f32_e32 v129, v152, v153
	v_mov_b32_e32 v131, v129
	s_nop 1
	v_permlane32_swap_b32_e32 v129, v131
	v_max_f32_e32 v129, v129, v131
	v_mfma_f32_32x32x16_bf16 a[16:31], v[132:135], v[140:143], a[16:31]
	v_max_f32_e32 v128, v128, v130
	v_mov_b32_e32 v130, v128
	s_nop 1
	v_permlane32_swap_b32_e32 v128, v130
	v_max_f32_e32 v128, v128, v130
	v_max_f32_e32 v130, v129, v129
	v_max_f32_e32 v131, v128, v128
	v_max_f32_e32 v130, v130, v131
	s_mov_b32 s0, 0x41000000
	v_mfma_f32_32x32x16_bf16 a[32:47], v[124:127], v[112:115], a[32:47]
	v_cmp_lt_f32_e32 vcc, s0, v130
	s_cmp_lg_u64 vcc, 0
	s_cselect_b64 s[0:1], -1, 0
	s_cbranch_vccnz .LBB0_41
	v_mov_b32_e32 v216, 1.0

.LBB0_17:
	v_mfma_f32_32x32x16_bf16 v[112:127], a[192:195], a[128:131], v[0:15]
	v_exp_f32_e32 v48, v48
	v_exp_f32_e32 v49, v49
	ds_read_b64_tr_b16 v[172:173], v215 offset:0
	v_cvt_pk_bf16_f32 v164, v128, v129
	v_mfma_f32_32x32x16_bf16 v[96:111], a[192:195], a[160:163], v[16:31]
	v_exp_f32_e32 v50, v50
	v_exp_f32_e32 v51, v51
	ds_read_b64_tr_b16 v[174:175], v215 offset:0x800
	v_cvt_pk_bf16_f32 v165, v130, v131
	v_mfma_f32_32x32x16_bf16 v[80:95], a[224:227], a[128:131], v[0:15]
	ds_read_b64_tr_b16 v[184:185], v215 offset:0x200
	v_exp_f32_e32 v239, v52
	v_exp_f32_e32 v240, v53
	v_cvt_pk_bf16_f32 v166, v132, v133
	v_mfma_f32_32x32x16_bf16 v[64:79], a[224:227], a[160:163], v[16:31]
	ds_read_b64_tr_b16 v[186:187], v215 offset:0xa00
	ds_read_b64_tr_b16 v[180:181], v215 offset:0x400
	v_exp_f32_e32 v241, v54
	v_exp_f32_e32 v242, v55
	v_cvt_pk_bf16_f32 v167, v134, v135
	v_mfma_f32_32x32x16_bf16 v[112:127], a[196:199], a[132:135], v[112:127]
	v_exp_f32_e32 v227, v56
	v_exp_f32_e32 v228, v57
	ds_read_b64_tr_b16 v[182:183], v215 offset:0xc00
	v_cvt_pk_bf16_f32 v128, v136, v137
	v_mfma_f32_32x32x16_bf16 v[96:111], a[196:199], a[164:167], v[96:111]
	v_exp_f32_e32 v229, v58
	v_exp_f32_e32 v230, v59
	ds_read_b64_tr_b16 v[188:189], v215 offset:0x600
	v_cvt_pk_bf16_f32 v129, v138, v139
	v_mfma_f32_32x32x16_bf16 v[80:95], a[228:231], a[132:135], v[80:95]
	v_exp_f32_e32 v231, v60
	v_exp_f32_e32 v232, v61
	ds_read_b64_tr_b16 v[190:191], v215 offset:0xe00
	v_cvt_pk_bf16_f32 v130, v140, v141
	v_mfma_f32_32x32x16_bf16 v[64:79], a[228:231], a[164:167], v[64:79]
	ds_read_b64_tr_b16 v[176:177], v215 offset:0x1000
	v_exp_f32_e32 v233, v62
	v_exp_f32_e32 v234, v63
	ds_read_b64_tr_b16 v[178:179], v215 offset:0x1800
	v_cvt_pk_bf16_f32 v131, v142, v143
	v_mfma_f32_32x32x16_bf16 v[112:127], a[200:203], a[136:139], v[112:127]
	v_exp_f32_e32 v141, v32
	v_exp_f32_e32 v142, v33
	ds_read_b64_tr_b16 v[168:169], v215 offset:0x1200
	v_cvt_pk_bf16_f32 v192, v144, v145
	v_mfma_f32_32x32x16_bf16 v[96:111], a[200:203], a[168:171], v[96:111]
	v_exp_f32_e32 v143, v34
	ds_read_b64_tr_b16 v[170:171], v215 offset:0x1a00
	v_exp_f32_e32 v243, v35
	v_cvt_pk_bf16_f32 v193, v146, v147
	v_mfma_f32_32x32x16_bf16 v[80:95], a[232:235], a[136:139], v[80:95]
	ds_read_b64_tr_b16 v[160:161], v215 offset:0x1400
	v_exp_f32_e32 v244, v36
	v_exp_f32_e32 v245, v37
	v_cvt_pk_bf16_f32 v194, v148, v149
	v_mfma_f32_32x32x16_bf16 v[64:79], a[232:235], a[168:171], v[64:79]
	ds_read_b64_tr_b16 v[162:163], v215 offset:0x1c00
	ds_read_b64_tr_b16 v[136:137], v215 offset:0x1600
	v_exp_f32_e32 v246, v38
	v_exp_f32_e32 v247, v39
	v_cvt_pk_bf16_f32 v195, v150, v151
	v_mfma_f32_32x32x16_bf16 v[112:127], a[204:207], a[140:143], v[112:127]
	v_exp_f32_e32 v148, v40
	v_exp_f32_e32 v149, v41
	ds_read_b64_tr_b16 v[138:139], v215 offset:0x1e00
	v_cvt_pk_bf16_f32 v144, v152, v153
	v_mfma_f32_32x32x16_bf16 v[96:111], a[204:207], a[172:175], v[96:111]
	v_exp_f32_e32 v150, v42
	v_exp_f32_e32 v151, v43
	ds_read_b64_tr_b16 v[132:133], v215 offset:0x2000
	v_cvt_pk_bf16_f32 v145, v154, v155
	v_mfma_f32_32x32x16_bf16 v[80:95], a[236:239], a[140:143], v[80:95]
	v_exp_f32_e32 v152, v44
	v_exp_f32_e32 v153, v45
	ds_read_b64_tr_b16 v[134:135], v215 offset:0x2800
	v_cvt_pk_bf16_f32 v146, v156, v157
	v_mfma_f32_32x32x16_bf16 v[64:79], a[236:239], a[172:175], v[64:79]
	ds_read_b64_tr_b16 v[60:61], v215 offset:0x2200
	v_exp_f32_e32 v154, v46
	v_exp_f32_e32 v155, v47
	ds_read_b64_tr_b16 v[62:63], v215 offset:0x2a00
	v_cvt_pk_bf16_f32 v147, v158, v159
	s_mov_b32 s0, s29
	v_mfma_f32_32x32x16_bf16 v[112:127], a[208:211], a[144:147], v[112:127]
	ds_read_b64_tr_b16 v[56:57], v215 offset:0x2400
	v_cvt_pk_bf16_f32 v52, v48, v49
	v_add_f32_e32 v32, v236, v48
	v_add_f32_e32 v33, v235, v49
	s_add_i32 s57, s58, s59
	s_and_b32 s57, s57, 0x7ffff
	s_mov_b32 s33, s57
	s_mov_b32 s1, s33
	v_mfma_f32_32x32x16_bf16 v[96:111], a[208:211], a[176:179], v[96:111]
	ds_read_b64_tr_b16 v[58:59], v215 offset:0x2c00
	v_cvt_pk_bf16_f32 v53, v50, v51
	v_add_f32_e32 v32, v32, v50
	v_add_f32_e32 v33, v33, v51
	s_mov_b32 s35, s20
	v_mfma_f32_32x32x16_bf16 v[80:95], a[240:243], a[144:147], v[80:95]
	ds_read_b64_tr_b16 v[48:49], v215 offset:0x2600
	v_cvt_pk_bf16_f32 v54, v239, v240
	v_add_f32_e32 v32, v32, v239
	v_add_f32_e32 v33, v33, v240
	s_add_i32 s36, s57, 0x400
	v_mfma_f32_32x32x16_bf16 v[64:79], a[240:243], a[176:179], v[64:79]
	ds_read_b64_tr_b16 v[50:51], v215 offset:0x2e00
	ds_read_b64_tr_b16 v[44:45], v215 offset:0x3000
	v_cvt_pk_bf16_f32 v55, v241, v242
	v_add_f32_e32 v32, v32, v241
	v_add_f32_e32 v33, v33, v242
	s_mov_b32 s37, s21
	v_mfma_f32_32x32x16_bf16 v[112:127], a[212:215], a[148:151], v[112:127]
	ds_read_b64_tr_b16 v[46:47], v215 offset:0x3800
	v_add_f32_e32 v32, v32, v227
	v_add_f32_e32 v33, v33, v228
	s_add_i32 s34, s57, 0x800
	s_mov_b32 s38, s34
	v_mfma_f32_32x32x16_bf16 v[96:111], a[212:215], a[180:183], v[96:111]
	ds_read_b64_tr_b16 v[40:41], v215 offset:0x3200
	v_add_f32_e32 v32, v32, v229
	v_add_f32_e32 v33, v33, v230
	s_mov_b32 s39, s22
	v_mfma_f32_32x32x16_bf16 v[80:95], a[244:247], a[148:151], v[80:95]
	ds_read_b64_tr_b16 v[42:43], v215 offset:0x3a00
	v_add_f32_e32 v32, v32, v231
	v_add_f32_e32 v33, v33, v232
	s_add_i32 s40, s57, 0xc00
	v_mfma_f32_32x32x16_bf16 v[64:79], a[244:247], a[180:183], v[64:79]
	ds_read_b64_tr_b16 v[36:37], v215 offset:0x3400
	ds_read_b64_tr_b16 v[38:39], v215 offset:0x3c00
	v_add_f32_e32 v156, v32, v233
	v_add_f32_e32 v157, v33, v234
	s_mov_b32 s41, s23
	v_mfma_f32_32x32x16_bf16 v[112:127], a[216:219], a[152:155], v[112:127]
	ds_read_b64_tr_b16 v[32:33], v215 offset:0x3600
	v_cvt_pk_bf16_f32 v140, v141, v142
	v_add_f32_e32 v158, v237, v141
	v_add_f32_e32 v142, v238, v142
	s_mov_b32 s42, s58
	v_mfma_f32_32x32x16_bf16 v[96:111], a[216:219], a[184:187], v[96:111]
	ds_read_b64_tr_b16 v[34:35], v215 offset:0x3e00
	v_cvt_pk_bf16_f32 v141, v143, v243
	v_add_f32_e32 v143, v158, v143
	v_add_f32_e32 v158, v142, v243
	v_mfma_f32_32x32x16_bf16 v[80:95], a[248:251], a[152:155], v[80:95]
	s_mov_b32 s43, s24
	v_cvt_pk_bf16_f32 v142, v244, v245
	v_add_f32_e32 v159, v143, v244
	v_add_f32_e32 v158, v158, v245
	v_mfma_f32_32x32x16_bf16 v[64:79], a[248:251], a[184:187], v[64:79]
	s_add_i32 s44, s58, 0x80
	v_cvt_pk_bf16_f32 v143, v246, v247
	v_add_f32_e32 v159, v159, v246
	v_add_f32_e32 v158, v158, v247
	v_mfma_f32_32x32x16_bf16 v[112:127], a[220:223], a[156:159], v[112:127]
	s_mov_b32 s45, s25
	v_add_f32_e32 v159, v159, v148
	v_add_f32_e32 v158, v158, v149
	v_mfma_f32_32x32x16_bf16 v[96:111], a[220:223], a[188:191], v[96:111]
	s_add_i32 s46, s58, 0x800
	v_add_f32_e32 v159, v159, v150
	v_add_f32_e32 v158, v158, v151
	v_mfma_f32_32x32x16_bf16 v[80:95], a[252:255], a[156:159], v[80:95]
	s_mov_b32 s47, s26
	v_add_f32_e32 v159, v159, v152
	v_add_f32_e32 v158, v158, v153
	v_mfma_f32_32x32x16_bf16 v[64:79], a[252:255], a[188:191], v[64:79]
	s_add_i32 s48, s58, 0x880
	v_add_f32_e32 v159, v159, v154
	v_add_f32_e32 v158, v158, v155
	v_add_f32_e32 v156, v156, v157
	s_waitcnt vmcnt(0) lgkmcnt(0)
	s_barrier
	s_mov_b32 m0, s0
	v_mfma_f32_32x32x16_bf16 a[0:15], v[172:175], v[164:167], a[0:15]
	v_mov_b32_e32 v157, v156
	buffer_load_dwordx4 v222, s[12:15], s1 offen lds
	s_mov_b32 m0, s35
	v_mfma_f32_32x32x16_bf16 a[16:31], v[172:175], v[192:195], a[16:31]
	v_permlane32_swap_b32_e32 v156, v157
	v_add_f32_e32 v156, v156, v157
	buffer_load_dwordx4 v223, s[12:15], s36 offen lds
	ds_read_b128 a[192:195], v217 offset:0
	s_mov_b32 m0, s37
	v_mfma_f32_32x32x16_bf16 a[32:47], v[184:187], v[164:167], a[32:47]
	v_add_f32_e32 v225, v225, v156
	v_add_f32_e32 v156, v159, v158
	v_mov_b32_e32 v157, v156
	buffer_load_dwordx4 v222, s[12:15], s38 offen lds
	ds_read_b128 a[196:199], v199 offset:0
	s_mov_b32 m0, s39
	v_mfma_f32_32x32x16_bf16 a[48:63], v[184:187], v[192:195], a[48:63]
	v_permlane32_swap_b32_e32 v156, v157
	v_add_f32_e32 v156, v156, v157
	buffer_load_dwordx4 v223, s[12:15], s40 offen lds
	ds_read_b128 a[200:203], v198 offset:0
	s_mov_b32 m0, s41
	v_mfma_f32_32x32x16_bf16 a[64:79], v[180:183], v[164:167], a[64:79]
	v_add_f32_e32 v226, v226, v156
	buffer_load_dwordx4 v196, s[4:7], s42 offen lds
	ds_read_b128 a[204:207], v197 offset:0
	s_mov_b32 m0, s43
	v_mfma_f32_32x32x16_bf16 a[80:95], v[180:183], v[192:195], a[80:95]
	buffer_load_dwordx4 v196, s[4:7], s44 offen lds
	ds_read_b128 a[208:211], v217 offset:128
	s_mov_b32 m0, s45
	v_mfma_f32_32x32x16_bf16 a[96:111], v[188:191], v[164:167], a[96:111]
	buffer_load_dwordx4 v196, s[4:7], s46 offen lds
	ds_read_b128 a[212:215], v199 offset:128
	s_mov_b32 m0, s47
	v_mfma_f32_32x32x16_bf16 a[112:127], v[188:191], v[192:195], a[112:127]
	buffer_load_dwordx4 v196, s[4:7], s48 offen lds
	ds_read_b128 a[216:219], v198 offset:128
	s_nop 0
	v_mfma_f32_32x32x16_bf16 a[0:15], v[176:179], v[128:131], a[0:15]
	ds_read_b128 a[220:223], v197 offset:128
	s_cmp_gt_u32 s27, 12
	s_cbranch_scc1 .Lka_done
	s_cmp_gt_u32 s27, 4
	s_cbranch_scc1 .Lka_single
	v_cvt_pk_bf16_f32 v248, v248, v249
	v_cvt_pk_bf16_f32 v249, v250, v251
	v_cvt_pk_bf16_f32 v250, v252, v253
	v_cvt_pk_bf16_f32 v251, v254, v255
	v_lshrrev_b32_e32 v252, 1, v208
	buffer_store_dwordx4 v[248:251], v252, s[12:15], s56 offen sc1
	v_mbcnt_lo_u32_b32 v253, -1, 0
	v_mbcnt_hi_u32_b32 v253, -1, v253
	v_lshlrev_b32_e32 v253, 4, v253
	v_add_u32_e32 v253, s84, v253
	ds_read_b128 v[248:251], v253
	ds_read_b128 v[252:255], v253 offset:1024
	s_cmp_eq_u32 s27, 2
	s_cbranch_scc0 .Lka_nopub
	s_cmp_eq_u32 s50, 0
	s_cbranch_scc0 .Lf1_pub_done
	v_mov_b32_e32 v210, s70
	s_mov_b64 exec, 1
	global_store_dword v209, v210, s[72:73] offset:3072 sc1
	s_mov_b64 exec, -1

.LBB0_19:
	s_waitcnt lgkmcnt(0)
	v_mfma_f32_32x32x16_bf16 v[112:127], a[192:195], a[128:131], v[0:15]
	v_exp_f32_e32 v80, v80
	v_exp_f32_e32 v81, v81
	ds_read_b64_tr_b16 v[180:181], v212 offset:0
	v_cvt_pk_bf16_f32 v168, v128, v129
	v_mfma_f32_32x32x16_bf16 v[96:111], a[192:195], a[160:163], v[16:31]
	v_exp_f32_e32 v82, v82
	v_exp_f32_e32 v83, v83
	ds_read_b64_tr_b16 v[182:183], v212 offset:0x800
	v_cvt_pk_bf16_f32 v169, v130, v131
	v_mfma_f32_32x32x16_bf16 v[48:63], a[224:227], a[128:131], v[0:15]
	ds_read_b64_tr_b16 v[184:185], v212 offset:0x200
	v_exp_f32_e32 v239, v84
	v_exp_f32_e32 v240, v85
	v_cvt_pk_bf16_f32 v170, v132, v133
	v_mfma_f32_32x32x16_bf16 v[32:47], a[224:227], a[160:163], v[16:31]
	ds_read_b64_tr_b16 v[186:187], v212 offset:0xa00
	ds_read_b64_tr_b16 v[176:177], v212 offset:0x400
	v_exp_f32_e32 v241, v86
	v_exp_f32_e32 v242, v87
	v_cvt_pk_bf16_f32 v171, v134, v135
	v_mfma_f32_32x32x16_bf16 v[112:127], a[196:199], a[132:135], v[112:127]
	v_exp_f32_e32 v227, v88
	v_exp_f32_e32 v228, v89
	ds_read_b64_tr_b16 v[178:179], v212 offset:0xc00
	v_cvt_pk_bf16_f32 v128, v136, v137
	v_mfma_f32_32x32x16_bf16 v[96:111], a[196:199], a[164:167], v[96:111]
	v_exp_f32_e32 v229, v90
	v_exp_f32_e32 v230, v91
	ds_read_b64_tr_b16 v[188:189], v212 offset:0x600
	v_cvt_pk_bf16_f32 v129, v138, v139
	v_mfma_f32_32x32x16_bf16 v[48:63], a[228:231], a[132:135], v[48:63]
	v_exp_f32_e32 v231, v92
	v_exp_f32_e32 v232, v93
	ds_read_b64_tr_b16 v[190:191], v212 offset:0xe00
	v_cvt_pk_bf16_f32 v130, v140, v141
	v_mfma_f32_32x32x16_bf16 v[32:47], a[228:231], a[164:167], v[32:47]
	ds_read_b64_tr_b16 v[172:173], v212 offset:0x1000
	v_exp_f32_e32 v233, v94
	v_exp_f32_e32 v234, v95
	ds_read_b64_tr_b16 v[174:175], v212 offset:0x1800
	v_cvt_pk_bf16_f32 v131, v142, v143
	v_mfma_f32_32x32x16_bf16 v[112:127], a[200:203], a[136:139], v[112:127]
	v_exp_f32_e32 v141, v64
	v_exp_f32_e32 v142, v65
	ds_read_b64_tr_b16 v[164:165], v212 offset:0x1200
	v_cvt_pk_bf16_f32 v192, v144, v145
	v_mfma_f32_32x32x16_bf16 v[96:111], a[200:203], a[168:171], v[96:111]
	v_exp_f32_e32 v143, v66
	ds_read_b64_tr_b16 v[166:167], v212 offset:0x1a00
	v_exp_f32_e32 v243, v67
	v_cvt_pk_bf16_f32 v193, v146, v147
	v_mfma_f32_32x32x16_bf16 v[48:63], a[232:235], a[136:139], v[48:63]
	ds_read_b64_tr_b16 v[160:161], v212 offset:0x1400
	v_exp_f32_e32 v244, v68
	v_exp_f32_e32 v245, v69
	v_cvt_pk_bf16_f32 v194, v148, v149
	v_mfma_f32_32x32x16_bf16 v[32:47], a[232:235], a[168:171], v[32:47]
	ds_read_b64_tr_b16 v[162:163], v212 offset:0x1c00
	ds_read_b64_tr_b16 v[136:137], v212 offset:0x1600
	v_exp_f32_e32 v246, v70
	v_exp_f32_e32 v247, v71
	v_cvt_pk_bf16_f32 v195, v150, v151
	v_mfma_f32_32x32x16_bf16 v[112:127], a[204:207], a[140:143], v[112:127]
	v_exp_f32_e32 v148, v72
	v_exp_f32_e32 v149, v73
	ds_read_b64_tr_b16 v[138:139], v212 offset:0x1e00
	v_cvt_pk_bf16_f32 v144, v152, v153
	v_mfma_f32_32x32x16_bf16 v[96:111], a[204:207], a[172:175], v[96:111]
	v_exp_f32_e32 v150, v74
	v_exp_f32_e32 v151, v75
	ds_read_b64_tr_b16 v[132:133], v212 offset:0x2000
	v_cvt_pk_bf16_f32 v145, v154, v155
	v_mfma_f32_32x32x16_bf16 v[48:63], a[236:239], a[140:143], v[48:63]
	v_exp_f32_e32 v152, v76
	v_exp_f32_e32 v153, v77
	ds_read_b64_tr_b16 v[134:135], v212 offset:0x2800
	v_cvt_pk_bf16_f32 v146, v156, v157
	v_mfma_f32_32x32x16_bf16 v[32:47], a[236:239], a[172:175], v[32:47]
	ds_read_b64_tr_b16 v[92:93], v212 offset:0x2200
	v_exp_f32_e32 v154, v78
	v_exp_f32_e32 v155, v79
	ds_read_b64_tr_b16 v[94:95], v212 offset:0x2a00
	v_cvt_pk_bf16_f32 v147, v158, v159
	s_mov_b32 s0, s3
	v_mfma_f32_32x32x16_bf16 v[112:127], a[208:211], a[144:147], v[112:127]
	ds_read_b64_tr_b16 v[88:89], v212 offset:0x2400
	v_cvt_pk_bf16_f32 v84, v80, v81
	v_add_f32_e32 v64, v236, v80
	v_add_f32_e32 v65, v235, v81
	s_add_i32 s58, s57, s60
	s_and_b32 s58, s58, 0x7ffff
	s_mov_b32 s1, s58
	v_mfma_f32_32x32x16_bf16 v[96:111], a[208:211], a[176:179], v[96:111]
	ds_read_b64_tr_b16 v[90:91], v212 offset:0x2c00
	v_cvt_pk_bf16_f32 v85, v82, v83
	v_add_f32_e32 v64, v64, v82
	v_add_f32_e32 v65, v65, v83
	s_mov_b32 s35, s10
	v_mfma_f32_32x32x16_bf16 v[48:63], a[240:243], a[144:147], v[48:63]
	ds_read_b64_tr_b16 v[80:81], v212 offset:0x2600
	v_cvt_pk_bf16_f32 v86, v239, v240
	v_add_f32_e32 v64, v64, v239
	v_add_f32_e32 v65, v65, v240
	s_add_i32 s36, s58, 0x400
	v_mfma_f32_32x32x16_bf16 v[32:47], a[240:243], a[176:179], v[32:47]
	ds_read_b64_tr_b16 v[82:83], v212 offset:0x2e00
	ds_read_b64_tr_b16 v[76:77], v212 offset:0x3000
	v_cvt_pk_bf16_f32 v87, v241, v242
	v_add_f32_e32 v64, v64, v241
	v_add_f32_e32 v65, v65, v242
	s_mov_b32 s37, s11
	v_mfma_f32_32x32x16_bf16 v[112:127], a[212:215], a[148:151], v[112:127]
	ds_read_b64_tr_b16 v[78:79], v212 offset:0x3800
	v_add_f32_e32 v64, v64, v227
	v_add_f32_e32 v65, v65, v228
	s_add_i32 s38, s58, 0x800
	v_mfma_f32_32x32x16_bf16 v[96:111], a[212:215], a[180:183], v[96:111]
	ds_read_b64_tr_b16 v[72:73], v212 offset:0x3200
	v_add_f32_e32 v64, v64, v229
	v_add_f32_e32 v65, v65, v230
	s_mov_b32 s39, s16
	v_mfma_f32_32x32x16_bf16 v[48:63], a[244:247], a[148:151], v[48:63]
	ds_read_b64_tr_b16 v[74:75], v212 offset:0x3a00
	v_add_f32_e32 v64, v64, v231
	v_add_f32_e32 v65, v65, v232
	s_add_i32 s40, s58, 0xc00
	v_mfma_f32_32x32x16_bf16 v[32:47], a[244:247], a[180:183], v[32:47]
	ds_read_b64_tr_b16 v[68:69], v212 offset:0x3400
	ds_read_b64_tr_b16 v[70:71], v212 offset:0x3c00
	v_add_f32_e32 v156, v64, v233
	v_add_f32_e32 v157, v65, v234
	s_mov_b32 s41, s2
	v_mfma_f32_32x32x16_bf16 v[112:127], a[216:219], a[152:155], v[112:127]
	ds_read_b64_tr_b16 v[64:65], v212 offset:0x3600
	v_cvt_pk_bf16_f32 v140, v141, v142
	v_add_f32_e32 v158, v237, v141
	v_add_f32_e32 v142, v238, v142
	v_mfma_f32_32x32x16_bf16 v[96:111], a[216:219], a[184:187], v[96:111]
	ds_read_b64_tr_b16 v[66:67], v212 offset:0x3e00
	v_cvt_pk_bf16_f32 v141, v143, v243
	v_add_f32_e32 v143, v158, v143
	v_add_f32_e32 v158, v142, v243
	v_mfma_f32_32x32x16_bf16 v[48:63], a[248:251], a[152:155], v[48:63]
	s_mov_b32 s42, s17
	v_cvt_pk_bf16_f32 v142, v244, v245
	v_add_f32_e32 v159, v143, v244
	v_add_f32_e32 v158, v158, v245
	v_mfma_f32_32x32x16_bf16 v[32:47], a[248:251], a[184:187], v[32:47]
	s_add_i32 s43, s57, 0x80
	v_cvt_pk_bf16_f32 v143, v246, v247
	v_add_f32_e32 v159, v159, v246
	v_add_f32_e32 v158, v158, v247
	v_mfma_f32_32x32x16_bf16 v[112:127], a[220:223], a[156:159], v[112:127]
	s_mov_b32 s44, s18
	v_add_f32_e32 v159, v159, v148
	v_add_f32_e32 v158, v158, v149
	v_mfma_f32_32x32x16_bf16 v[96:111], a[220:223], a[188:191], v[96:111]
	v_add_f32_e32 v159, v159, v150
	v_add_f32_e32 v158, v158, v151
	v_mfma_f32_32x32x16_bf16 v[48:63], a[252:255], a[156:159], v[48:63]
	s_mov_b32 s45, s19
	v_add_f32_e32 v159, v159, v152
	v_add_f32_e32 v158, v158, v153
	v_mfma_f32_32x32x16_bf16 v[32:47], a[252:255], a[188:191], v[32:47]
	s_add_i32 s46, s57, 0x880
	v_add_f32_e32 v159, v159, v154
	v_add_f32_e32 v158, v158, v155
	v_add_f32_e32 v156, v156, v157
	s_waitcnt vmcnt(0) lgkmcnt(0)
	s_barrier
	s_mov_b32 m0, s0
	v_mfma_f32_32x32x16_bf16 a[0:15], v[180:183], v[168:171], a[0:15]
	v_mov_b32_e32 v157, v156
	buffer_load_dwordx4 v222, s[12:15], s1 offen lds
	s_mov_b32 m0, s35
	v_mfma_f32_32x32x16_bf16 a[16:31], v[180:183], v[192:195], a[16:31]
	v_permlane32_swap_b32_e32 v156, v157
	v_add_f32_e32 v156, v156, v157
	buffer_load_dwordx4 v223, s[12:15], s36 offen lds
	ds_read_b128 a[192:195], v218 offset:0
	s_mov_b32 m0, s37
	v_mfma_f32_32x32x16_bf16 a[32:47], v[184:187], v[168:171], a[32:47]
	v_add_f32_e32 v225, v225, v156
	v_add_f32_e32 v156, v159, v158
	v_mov_b32_e32 v157, v156
	buffer_load_dwordx4 v222, s[12:15], s38 offen lds
	ds_read_b128 a[196:199], v219 offset:0
	s_mov_b32 m0, s39
	v_mfma_f32_32x32x16_bf16 a[48:63], v[184:187], v[192:195], a[48:63]
	v_permlane32_swap_b32_e32 v156, v157
	v_add_f32_e32 v156, v156, v157
	buffer_load_dwordx4 v223, s[12:15], s40 offen lds
	ds_read_b128 a[200:203], v220 offset:0
	s_mov_b32 m0, s41
	v_mfma_f32_32x32x16_bf16 a[64:79], v[176:179], v[168:171], a[64:79]
	v_add_f32_e32 v226, v226, v156
	buffer_load_dwordx4 v196, s[4:7], s33 offen lds
	ds_read_b128 a[204:207], v221 offset:0
	s_mov_b32 m0, s42
	v_mfma_f32_32x32x16_bf16 a[80:95], v[176:179], v[192:195], a[80:95]
	buffer_load_dwordx4 v196, s[4:7], s43 offen lds
	ds_read_b128 a[208:211], v218 offset:128
	s_mov_b32 m0, s44
	v_mfma_f32_32x32x16_bf16 a[96:111], v[188:191], v[168:171], a[96:111]
	buffer_load_dwordx4 v196, s[4:7], s34 offen lds
	ds_read_b128 a[212:215], v219 offset:128
	s_mov_b32 m0, s45
	v_mfma_f32_32x32x16_bf16 a[112:127], v[188:191], v[192:195], a[112:127]
	buffer_load_dwordx4 v196, s[4:7], s46 offen lds
	ds_read_b128 a[216:219], v220 offset:128
	s_nop 0
	v_mfma_f32_32x32x16_bf16 a[0:15], v[172:175], v[128:131], a[0:15]
	ds_read_b128 a[220:223], v221 offset:128
	s_cmp_gt_u32 s27, 12
	s_cbranch_scc1 .Lkc_done
	s_cmp_gt_u32 s27, 4
	s_cbranch_scc1 .Lkc_single
	v_cvt_pk_bf16_f32 v248, v248, v249
	v_cvt_pk_bf16_f32 v249, v250, v251
	v_cvt_pk_bf16_f32 v250, v252, v253
	v_cvt_pk_bf16_f32 v251, v254, v255
	v_lshrrev_b32_e32 v252, 1, v208
	buffer_store_dwordx4 v[248:251], v252, s[12:15], s56 offen sc1
	v_mbcnt_lo_u32_b32 v253, -1, 0
	v_mbcnt_hi_u32_b32 v253, -1, v253
	v_lshlrev_b32_e32 v253, 4, v253
	v_add_u32_e32 v253, s84, v253
	ds_read_b128 v[248:251], v253
	ds_read_b128 v[252:255], v253 offset:1024
	s_branch .Lkc_done

.LBB0_36:
	s_lshl_b32 s53, s50, 6
	s_add_i32 s53, s53, s52
	v_mov_b32_e32 v200, s53
	s_lshl_b32 s53, s50, 14
	s_add_i32 s53, s53, 0x10000
	v_mov_b32_e32 v201, s53
	v_mbcnt_lo_u32_b32 v204, -1, 0
	v_mbcnt_hi_u32_b32 v204, -1, v204
	v_lshrrev_b32_e32 v202, 4, v204
	v_add_u32_e32 v203, 4, v202
	v_add_u32_e32 v205, 8, v202
	v_add_u32_e32 v206, 12, v202
	v_add_u32_e32 v207, 16, v202
	v_add_u32_e32 v208, 20, v202
	v_add_u32_e32 v209, 24, v202
	v_add_u32_e32 v210, 28, v202
	v_mfma_f32_32x32x16_bf16 v[112:127], a[192:195], a[128:131], v[0:15]
	v_exp_f32_e32 v48, v48
	v_exp_f32_e32 v49, v49
	ds_read_b64_tr_b16 v[180:181], v215 offset:0
	v_cvt_pk_bf16_f32 v164, v128, v129
	v_mfma_f32_32x32x16_bf16 v[96:111], a[192:195], a[160:163], v[16:31]
	v_exp_f32_e32 v50, v50
	v_exp_f32_e32 v51, v51
	ds_read_b64_tr_b16 v[182:183], v215 offset:0x800
	v_cvt_pk_bf16_f32 v165, v130, v131
	v_mfma_f32_32x32x16_bf16 v[80:95], a[224:227], a[128:131], v[0:15]
	v_exp_f32_e32 v218, v52
	v_exp_f32_e32 v219, v53
	ds_read_b64_tr_b16 v[188:189], v215 offset:0x200
	v_cvt_pk_bf16_f32 v166, v132, v133
	v_mfma_f32_32x32x16_bf16 v[64:79], a[224:227], a[160:163], v[16:31]
	ds_read_b64_tr_b16 v[190:191], v215 offset:0xa00
	ds_read_b64_tr_b16 v[176:177], v215 offset:0x400
	v_exp_f32_e32 v230, v54
	v_exp_f32_e32 v231, v55
	v_cvt_pk_bf16_f32 v167, v134, v135
	v_mfma_f32_32x32x16_bf16 v[112:127], a[196:199], a[132:135], v[112:127]
	v_exp_f32_e32 v220, v56
	v_exp_f32_e32 v221, v57
	ds_read_b64_tr_b16 v[178:179], v215 offset:0xc00
	v_cvt_pk_bf16_f32 v128, v136, v137
	v_mfma_f32_32x32x16_bf16 v[96:111], a[196:199], a[164:167], v[96:111]
	v_exp_f32_e32 v222, v58
	v_exp_f32_e32 v223, v59
	ds_read_b64_tr_b16 v[184:185], v215 offset:0x600
	v_cvt_pk_bf16_f32 v129, v138, v139
	v_mfma_f32_32x32x16_bf16 v[80:95], a[228:231], a[132:135], v[80:95]
	v_exp_f32_e32 v224, v60
	v_exp_f32_e32 v227, v61
	ds_read_b64_tr_b16 v[186:187], v215 offset:0xe00
	v_cvt_pk_bf16_f32 v130, v140, v141
	v_mfma_f32_32x32x16_bf16 v[64:79], a[228:231], a[164:167], v[64:79]
	ds_read_b64_tr_b16 v[172:173], v215 offset:0x1000
	v_exp_f32_e32 v228, v62
	v_exp_f32_e32 v229, v63
	ds_read_b64_tr_b16 v[174:175], v215 offset:0x1800
	v_cvt_pk_bf16_f32 v131, v142, v143
	v_mfma_f32_32x32x16_bf16 v[112:127], a[200:203], a[136:139], v[112:127]
	v_exp_f32_e32 v141, v32
	v_exp_f32_e32 v142, v33
	ds_read_b64_tr_b16 v[168:169], v215 offset:0x1200
	v_cvt_pk_bf16_f32 v192, v144, v145
	v_mfma_f32_32x32x16_bf16 v[96:111], a[200:203], a[168:171], v[96:111]
	v_exp_f32_e32 v143, v34
	ds_read_b64_tr_b16 v[170:171], v215 offset:0x1a00
	v_exp_f32_e32 v232, v35
	v_cvt_pk_bf16_f32 v193, v146, v147
	v_mfma_f32_32x32x16_bf16 v[80:95], a[232:235], a[136:139], v[80:95]
	ds_read_b64_tr_b16 v[160:161], v215 offset:0x1400
	v_exp_f32_e32 v233, v36
	v_exp_f32_e32 v234, v37
	v_cvt_pk_bf16_f32 v194, v148, v149
	v_mfma_f32_32x32x16_bf16 v[64:79], a[232:235], a[168:171], v[64:79]
	ds_read_b64_tr_b16 v[162:163], v215 offset:0x1c00
	ds_read_b64_tr_b16 v[136:137], v215 offset:0x1600
	v_exp_f32_e32 v239, v38
	v_exp_f32_e32 v240, v39
	v_cvt_pk_bf16_f32 v195, v150, v151
	v_mfma_f32_32x32x16_bf16 v[112:127], a[204:207], a[140:143], v[112:127]
	v_exp_f32_e32 v148, v40
	v_exp_f32_e32 v149, v41
	ds_read_b64_tr_b16 v[138:139], v215 offset:0x1e00
	v_cvt_pk_bf16_f32 v144, v152, v153
	v_mfma_f32_32x32x16_bf16 v[96:111], a[204:207], a[172:175], v[96:111]
	v_exp_f32_e32 v150, v42
	v_exp_f32_e32 v151, v43
	ds_read_b64_tr_b16 v[132:133], v215 offset:0x2000
	v_cvt_pk_bf16_f32 v145, v154, v155
	v_mfma_f32_32x32x16_bf16 v[80:95], a[236:239], a[140:143], v[80:95]
	v_exp_f32_e32 v152, v44
	v_exp_f32_e32 v153, v45
	ds_read_b64_tr_b16 v[134:135], v215 offset:0x2800
	v_cvt_pk_bf16_f32 v146, v156, v157
	v_mfma_f32_32x32x16_bf16 v[64:79], a[236:239], a[172:175], v[64:79]
	ds_read_b64_tr_b16 v[60:61], v215 offset:0x2200
	v_exp_f32_e32 v154, v46
	v_exp_f32_e32 v155, v47
	ds_read_b64_tr_b16 v[62:63], v215 offset:0x2a00
	v_cvt_pk_bf16_f32 v147, v158, v159
	v_mfma_f32_32x32x16_bf16 v[112:127], a[208:211], a[144:147], v[112:127]
	ds_read_b64_tr_b16 v[56:57], v215 offset:0x2400
	v_cvt_pk_bf16_f32 v52, v48, v49
	v_add_f32_e32 v32, v236, v48
	v_add_f32_e32 v33, v235, v49
	s_add_i32 s12, s28, 0x80000
	s_mov_b32 s0, s12
	v_mfma_f32_32x32x16_bf16 v[96:111], a[208:211], a[176:179], v[96:111]
	ds_read_b64_tr_b16 v[58:59], v215 offset:0x2c00
	v_cvt_pk_bf16_f32 v53, v50, v51
	v_add_f32_e32 v32, v32, v50
	v_add_f32_e32 v33, v33, v51
	v_mfma_f32_32x32x16_bf16 v[80:95], a[240:243], a[144:147], v[80:95]
	ds_read_b64_tr_b16 v[48:49], v215 offset:0x2600
	v_cvt_pk_bf16_f32 v54, v218, v219
	v_add_f32_e32 v32, v32, v218
	v_add_f32_e32 v33, v33, v219
	s_add_i32 s1, s28, 0x80400
	v_mfma_f32_32x32x16_bf16 v[64:79], a[240:243], a[176:179], v[64:79]
	ds_read_b64_tr_b16 v[50:51], v215 offset:0x2e00
	ds_read_b64_tr_b16 v[44:45], v215 offset:0x3000
	v_cvt_pk_bf16_f32 v55, v230, v231
	v_add_f32_e32 v32, v32, v230
	v_add_f32_e32 v33, v33, v231
	v_mfma_f32_32x32x16_bf16 v[112:127], a[212:215], a[148:151], v[112:127]
	ds_read_b64_tr_b16 v[46:47], v215 offset:0x3800
	v_add_f32_e32 v32, v32, v220
	v_add_f32_e32 v33, v33, v221
	s_add_i32 s13, s28, 0x80800
	s_mov_b32 s14, s13
	v_mfma_f32_32x32x16_bf16 v[96:111], a[212:215], a[180:183], v[96:111]
	ds_read_b64_tr_b16 v[40:41], v215 offset:0x3200
	v_add_f32_e32 v32, v32, v222
	v_add_f32_e32 v33, v33, v223
	v_mfma_f32_32x32x16_bf16 v[80:95], a[244:247], a[148:151], v[80:95]
	ds_read_b64_tr_b16 v[42:43], v215 offset:0x3a00
	v_add_f32_e32 v32, v32, v224
	v_add_f32_e32 v33, v33, v227
	s_add_i32 s15, s28, 0x80c00
	v_mfma_f32_32x32x16_bf16 v[64:79], a[244:247], a[180:183], v[64:79]
	ds_read_b64_tr_b16 v[36:37], v215 offset:0x3400
	ds_read_b64_tr_b16 v[38:39], v215 offset:0x3c00
	v_add_f32_e32 v156, v32, v228
	v_add_f32_e32 v157, v33, v229
	v_mfma_f32_32x32x16_bf16 v[112:127], a[216:219], a[152:155], v[112:127]
	ds_read_b64_tr_b16 v[32:33], v215 offset:0x3600
	v_cvt_pk_bf16_f32 v140, v141, v142
	v_add_f32_e32 v158, v237, v141
	v_add_f32_e32 v142, v238, v142
	s_add_i32 s27, s88, 0x0
	v_mfma_f32_32x32x16_bf16 v[96:111], a[216:219], a[184:187], v[96:111]
	ds_read_b64_tr_b16 v[34:35], v215 offset:0x3e00
	v_cvt_pk_bf16_f32 v141, v143, v232
	v_add_f32_e32 v143, v158, v143
	v_add_f32_e32 v158, v142, v232
	v_mfma_f32_32x32x16_bf16 v[80:95], a[248:251], a[152:155], v[80:95]
	v_cvt_pk_bf16_f32 v142, v233, v234
	v_add_f32_e32 v159, v143, v233
	v_add_f32_e32 v158, v158, v234
	v_mfma_f32_32x32x16_bf16 v[64:79], a[248:251], a[184:187], v[64:79]
	s_add_i32 s30, s88, 0x80
	v_cvt_pk_bf16_f32 v143, v239, v240
	v_add_f32_e32 v159, v159, v239
	v_add_f32_e32 v158, v158, v240
	v_mfma_f32_32x32x16_bf16 v[112:127], a[220:223], a[156:159], v[112:127]
	v_add_f32_e32 v159, v159, v148
	v_add_f32_e32 v158, v158, v149
	v_mfma_f32_32x32x16_bf16 v[96:111], a[220:223], a[188:191], v[96:111]
	s_add_i32 s31, s88, 0x800
	v_add_f32_e32 v159, v159, v150
	v_add_f32_e32 v158, v158, v151
	v_mfma_f32_32x32x16_bf16 v[80:95], a[252:255], a[156:159], v[80:95]
	v_add_f32_e32 v159, v159, v152
	v_add_f32_e32 v158, v158, v153
	v_mfma_f32_32x32x16_bf16 v[64:79], a[252:255], a[188:191], v[64:79]
	s_add_i32 s33, s88, 0x880
	v_add_f32_e32 v159, v159, v154
	v_add_f32_e32 v158, v158, v155
	v_add_f32_e32 v156, v156, v157
	s_waitcnt vmcnt(0) lgkmcnt(0)
	s_barrier
	v_mfma_f32_32x32x16_bf16 a[0:15], v[180:183], v[164:167], a[0:15]
	v_mov_b32_e32 v157, v156
	v_mfma_f32_32x32x16_bf16 a[16:31], v[180:183], v[192:195], a[16:31]
	s_nop 1
	v_permlane32_swap_b32_e32 v156, v157
	v_add_f32_e32 v156, v156, v157
	ds_read_b128 a[192:195], v217 offset:0
	v_mfma_f32_32x32x16_bf16 a[32:47], v[188:191], v[164:167], a[32:47]
	v_add_f32_e32 v219, v225, v156
	v_add_f32_e32 v156, v159, v158
	v_mov_b32_e32 v157, v156
	ds_read_b128 a[196:199], v199 offset:0
	v_mfma_f32_32x32x16_bf16 a[48:63], v[188:191], v[192:195], a[48:63]
	v_permlane32_swap_b32_e32 v156, v157
	v_add_f32_e32 v156, v156, v157
	ds_read_b128 a[200:203], v198 offset:0
	s_mov_b32 m0, s23
	v_mfma_f32_32x32x16_bf16 a[64:79], v[176:179], v[164:167], a[64:79]
	v_add_f32_e32 v218, v226, v156
	buffer_load_dwordx4 v196, s[4:7], s27 offen lds
	ds_read_b128 a[204:207], v197 offset:0
	s_mov_b32 m0, s24
	v_mfma_f32_32x32x16_bf16 a[80:95], v[176:179], v[192:195], a[80:95]
	buffer_load_dwordx4 v196, s[4:7], s30 offen lds
	ds_read_b128 a[208:211], v217 offset:128
	s_mov_b32 m0, s25
	v_mfma_f32_32x32x16_bf16 a[96:111], v[184:187], v[164:167], a[96:111]
	buffer_load_dwordx4 v196, s[4:7], s31 offen lds
	ds_read_b128 a[212:215], v199 offset:128
	s_mov_b32 m0, s26
	v_mfma_f32_32x32x16_bf16 a[112:127], v[184:187], v[192:195], a[112:127]
	buffer_load_dwordx4 v196, s[4:7], s33 offen lds
	ds_read_b128 a[216:219], v198 offset:128
	v_mfma_f32_32x32x16_bf16 a[0:15], v[172:175], v[128:131], a[0:15]
	ds_read_b128 a[220:223], v197 offset:128
	v_max3_f32 v156, v112, v113, v80
	v_max3_f32 v157, v114, v115, v81
	v_max3_f32 v156, v156, v82, v83
	v_mfma_f32_32x32x16_bf16 a[16:31], v[172:175], v[144:147], a[16:31]
	ds_read_b128 a[224:227], v217 offset:8192
	v_max3_f32 v156, v156, v116, v117
	v_max3_f32 v157, v157, v118, v119
	v_max3_f32 v156, v156, v84, v85
	v_max3_f32 v157, v157, v86, v87
	v_mfma_f32_32x32x16_bf16 a[32:47], v[168:171], v[128:131], a[32:47]
	ds_read_b128 a[228:231], v199 offset:8192
	v_max3_f32 v156, v156, v120, v121
	v_max3_f32 v157, v157, v122, v123
	v_max3_f32 v156, v156, v88, v89
	v_max3_f32 v157, v157, v90, v91
	v_mfma_f32_32x32x16_bf16 a[48:63], v[168:171], v[144:147], a[48:63]
	ds_read_b128 a[232:235], v198 offset:8192
	v_max3_f32 v156, v156, v124, v125
	v_max3_f32 v157, v157, v126, v127
	v_max3_f32 v156, v156, v92, v93
	v_max3_f32 v157, v157, v94, v95
	v_mfma_f32_32x32x16_bf16 a[64:79], v[160:163], v[128:131], a[64:79]
	ds_read_b128 a[236:239], v197 offset:8192
	v_max3_f32 v158, v96, v97, v64
	v_max3_f32 v159, v98, v99, v65
	v_max3_f32 v158, v158, v66, v67
	v_mfma_f32_32x32x16_bf16 a[80:95], v[160:163], v[144:147], a[80:95]
	ds_read_b128 a[240:243], v217 offset:8320
	v_max3_f32 v158, v158, v100, v101
	v_max3_f32 v159, v159, v102, v103
	v_max3_f32 v158, v158, v68, v69
	v_max3_f32 v159, v159, v70, v71
	v_mfma_f32_32x32x16_bf16 a[96:111], v[136:139], v[128:131], a[96:111]
	ds_read_b128 a[244:247], v199 offset:8320
	v_max3_f32 v128, v158, v104, v105
	v_max3_f32 v129, v159, v106, v107
	v_max3_f32 v128, v128, v72, v73
	v_max3_f32 v129, v129, v74, v75
	v_mfma_f32_32x32x16_bf16 a[112:127], v[136:139], v[144:147], a[112:127]
	ds_read_b128 a[248:251], v198 offset:8320
	v_max3_f32 v128, v128, v108, v109
	v_max3_f32 v129, v129, v110, v111
	v_max3_f32 v128, v128, v76, v77
	v_max3_f32 v130, v129, v78, v79
	v_mfma_f32_32x32x16_bf16 a[0:15], v[132:135], v[52:55], a[0:15]
	ds_read_b128 a[252:255], v197 offset:8320
	v_max_f32_e32 v129, v156, v157
	v_mov_b32_e32 v131, v129
	s_nop 1
	v_permlane32_swap_b32_e32 v129, v131
	v_max_f32_e32 v129, v129, v131
	v_mfma_f32_32x32x16_bf16 a[16:31], v[132:135], v[140:143], a[16:31]
	v_max_f32_e32 v128, v128, v130
	v_mov_b32_e32 v130, v128
	s_nop 1
	v_permlane32_swap_b32_e32 v128, v130
	v_max_f32_e32 v128, v128, v130
	v_max_f32_e32 v130, v129, v129
	v_max_f32_e32 v131, v128, v128
	v_max_f32_e32 v130, v130, v131
	s_mov_b32 s0, 0x41000000
	v_mfma_f32_32x32x16_bf16 a[32:47], v[60:63], v[52:55], a[32:47]
	v_cmp_lt_f32_e32 vcc, s0, v130
	s_cmp_lg_u64 vcc, 0
	s_cselect_b64 s[0:1], -1, 0
	s_cbranch_vccnz .LBB0_43

.LBB0_38:
	s_waitcnt lgkmcnt(0)
	v_mfma_f32_32x32x16_bf16 v[112:127], a[192:195], a[128:131], v[0:15]
	ds_read_b64_tr_b16 v[172:173], v212 offset:0
	v_exp_f32_e32 v227, v80
	v_exp_f32_e32 v228, v81
	v_cvt_pk_bf16_f32 v164, v128, v129
	v_mfma_f32_32x32x16_bf16 v[96:111], a[192:195], a[160:163], v[16:31]
	v_exp_f32_e32 v82, v82
	v_exp_f32_e32 v83, v83
	ds_read_b64_tr_b16 v[174:175], v212 offset:0x800
	v_cvt_pk_bf16_f32 v165, v130, v131
	v_mfma_f32_32x32x16_bf16 v[48:63], a[224:227], a[128:131], v[0:15]
	v_exp_f32_e32 v84, v84
	v_exp_f32_e32 v85, v85
	ds_read_b64_tr_b16 v[180:181], v212 offset:0x200
	v_cvt_pk_bf16_f32 v166, v132, v133
	v_mfma_f32_32x32x16_bf16 v[32:47], a[224:227], a[160:163], v[16:31]
	ds_read_b64_tr_b16 v[182:183], v212 offset:0xa00
	v_exp_f32_e32 v86, v86
	v_exp_f32_e32 v87, v87
	ds_read_b64_tr_b16 v[184:185], v212 offset:0x400
	v_cvt_pk_bf16_f32 v167, v134, v135
	v_mfma_f32_32x32x16_bf16 v[112:127], a[196:199], a[132:135], v[112:127]
	v_exp_f32_e32 v80, v88
	v_exp_f32_e32 v81, v89
	ds_read_b64_tr_b16 v[186:187], v212 offset:0xc00
	v_cvt_pk_bf16_f32 v160, v136, v137
	v_mfma_f32_32x32x16_bf16 v[96:111], a[196:199], a[164:167], v[96:111]
	v_exp_f32_e32 v90, v90
	v_exp_f32_e32 v91, v91
	ds_read_b64_tr_b16 v[192:193], v212 offset:0x600
	v_cvt_pk_bf16_f32 v161, v138, v139
	v_mfma_f32_32x32x16_bf16 v[48:63], a[228:231], a[132:135], v[48:63]
	v_exp_f32_e32 v217, v92
	v_exp_f32_e32 v220, v93
	ds_read_b64_tr_b16 v[194:195], v212 offset:0xe00
	v_cvt_pk_bf16_f32 v162, v140, v141
	v_mfma_f32_32x32x16_bf16 v[32:47], a[228:231], a[164:167], v[32:47]
	ds_read_b64_tr_b16 v[188:189], v212 offset:0x1000
	v_exp_f32_e32 v221, v94
	v_exp_f32_e32 v222, v95
	ds_read_b64_tr_b16 v[190:191], v212 offset:0x1800
	v_cvt_pk_bf16_f32 v163, v142, v143
	v_mfma_f32_32x32x16_bf16 v[112:127], a[200:203], a[136:139], v[112:127]
	v_exp_f32_e32 v130, v64
	v_exp_f32_e32 v131, v65
	ds_read_b64_tr_b16 v[176:177], v212 offset:0x1200
	v_cvt_pk_bf16_f32 v196, v144, v145
	v_mfma_f32_32x32x16_bf16 v[96:111], a[200:203], a[168:171], v[96:111]
	v_exp_f32_e32 v138, v66
	v_exp_f32_e32 v139, v67
	ds_read_b64_tr_b16 v[178:179], v212 offset:0x1a00
	v_cvt_pk_bf16_f32 v197, v146, v147
	v_mfma_f32_32x32x16_bf16 v[48:63], a[232:235], a[136:139], v[48:63]
	ds_read_b64_tr_b16 v[168:169], v212 offset:0x1400
	v_exp_f32_e32 v229, v68
	v_exp_f32_e32 v230, v69
	v_cvt_pk_bf16_f32 v198, v148, v149
	v_mfma_f32_32x32x16_bf16 v[32:47], a[232:235], a[168:171], v[32:47]
	ds_read_b64_tr_b16 v[170:171], v212 offset:0x1c00
	ds_read_b64_tr_b16 v[144:145], v212 offset:0x1600
	v_exp_f32_e32 v231, v70
	v_exp_f32_e32 v232, v71
	v_cvt_pk_bf16_f32 v199, v150, v151
	v_mfma_f32_32x32x16_bf16 v[112:127], a[204:207], a[140:143], v[112:127]
	v_exp_f32_e32 v64, v72
	v_exp_f32_e32 v65, v73
	ds_read_b64_tr_b16 v[146:147], v212 offset:0x1e00
	v_cvt_pk_bf16_f32 v148, v152, v153
	v_mfma_f32_32x32x16_bf16 v[96:111], a[204:207], a[172:175], v[96:111]
	v_exp_f32_e32 v70, v74
	v_exp_f32_e32 v71, v75
	ds_read_b64_tr_b16 v[140:141], v212 offset:0x2000
	v_cvt_pk_bf16_f32 v149, v154, v155
	v_mfma_f32_32x32x16_bf16 v[48:63], a[236:239], a[140:143], v[48:63]
	v_exp_f32_e32 v154, v76
	v_exp_f32_e32 v155, v77
	ds_read_b64_tr_b16 v[142:143], v212 offset:0x2800
	v_cvt_pk_bf16_f32 v150, v156, v157
	v_mfma_f32_32x32x16_bf16 v[32:47], a[236:239], a[172:175], v[32:47]
	ds_read_b64_tr_b16 v[66:67], v212 offset:0x2200
	v_exp_f32_e32 v156, v78
	v_exp_f32_e32 v157, v79
	ds_read_b64_tr_b16 v[68:69], v212 offset:0x2a00
	v_cvt_pk_bf16_f32 v151, v158, v159
	v_mfma_f32_32x32x16_bf16 v[112:127], a[208:211], a[144:147], v[112:127]
	ds_read_b64_tr_b16 v[132:133], v212 offset:0x2400
	v_cvt_pk_bf16_f32 v72, v227, v228
	v_add_f32_e32 v74, v226, v227
	v_add_f32_e32 v75, v224, v228
	s_add_i32 s0, s28, 0x84000
	v_mfma_f32_32x32x16_bf16 v[96:111], a[208:211], a[176:179], v[96:111]
	ds_read_b64_tr_b16 v[134:135], v212 offset:0x2c00
	v_cvt_pk_bf16_f32 v73, v82, v83
	v_add_f32_e32 v78, v74, v82
	v_add_f32_e32 v75, v75, v83
	v_mfma_f32_32x32x16_bf16 v[48:63], a[240:243], a[144:147], v[48:63]
	ds_read_b64_tr_b16 v[76:77], v212 offset:0x2600
	v_cvt_pk_bf16_f32 v74, v84, v85
	v_add_f32_e32 v84, v78, v84
	v_add_f32_e32 v85, v75, v85
	s_add_i32 s1, s28, 0x84400
	v_mfma_f32_32x32x16_bf16 v[32:47], a[240:243], a[176:179], v[32:47]
	ds_read_b64_tr_b16 v[78:79], v212 offset:0x2e00
	ds_read_b64_tr_b16 v[82:83], v212 offset:0x3000
	v_cvt_pk_bf16_f32 v75, v86, v87
	v_add_f32_e32 v86, v84, v86
	v_add_f32_e32 v87, v85, v87
	v_mfma_f32_32x32x16_bf16 v[112:127], a[212:215], a[148:151], v[112:127]
	ds_read_b64_tr_b16 v[84:85], v212 offset:0x3800
	v_add_f32_e32 v88, v86, v80
	v_add_f32_e32 v89, v87, v81
	s_add_i32 s4, s28, 0x84800
	v_mfma_f32_32x32x16_bf16 v[96:111], a[212:215], a[180:183], v[96:111]
	ds_read_b64_tr_b16 v[86:87], v212 offset:0x3200
	v_add_f32_e32 v92, v88, v90
	v_add_f32_e32 v93, v89, v91
	v_mfma_f32_32x32x16_bf16 v[48:63], a[244:247], a[148:151], v[48:63]
	ds_read_b64_tr_b16 v[88:89], v212 offset:0x3a00
	v_add_f32_e32 v128, v92, v217
	v_add_f32_e32 v129, v93, v220
	s_add_i32 s5, s28, 0x84c00
	v_mfma_f32_32x32x16_bf16 v[32:47], a[244:247], a[180:183], v[32:47]
	ds_read_b64_tr_b16 v[92:93], v212 offset:0x3400
	ds_read_b64_tr_b16 v[94:95], v212 offset:0x3c00
	v_add_f32_e32 v152, v128, v221
	v_add_f32_e32 v153, v129, v222
	v_mfma_f32_32x32x16_bf16 v[112:127], a[216:219], a[152:155], v[112:127]
	ds_read_b64_tr_b16 v[128:129], v212 offset:0x3600
	v_cvt_pk_bf16_f32 v136, v130, v131
	v_add_f32_e32 v158, v223, v130
	v_add_f32_e32 v159, v225, v131
	v_mfma_f32_32x32x16_bf16 v[96:111], a[216:219], a[184:187], v[96:111]
	ds_read_b64_tr_b16 v[130:131], v212 offset:0x3e00
	v_cvt_pk_bf16_f32 v137, v138, v139
	v_add_f32_e32 v158, v158, v138
	v_add_f32_e32 v139, v159, v139
	v_mfma_f32_32x32x16_bf16 v[48:63], a[248:251], a[152:155], v[48:63]
	v_cvt_pk_bf16_f32 v138, v229, v230
	v_add_f32_e32 v158, v158, v229
	v_add_f32_e32 v159, v139, v230
	v_mfma_f32_32x32x16_bf16 v[32:47], a[248:251], a[184:187], v[32:47]
	s_add_i32 s6, s28, 0x80080
	v_cvt_pk_bf16_f32 v139, v231, v232
	v_add_f32_e32 v158, v158, v231
	v_add_f32_e32 v159, v159, v232
	v_mfma_f32_32x32x16_bf16 v[112:127], a[220:223], a[156:159], v[112:127]
	v_add_f32_e32 v158, v158, v64
	v_add_f32_e32 v159, v159, v65
	v_mfma_f32_32x32x16_bf16 v[96:111], a[220:223], a[188:191], v[96:111]
	v_add_f32_e32 v158, v158, v70
	v_add_f32_e32 v159, v159, v71
	v_mfma_f32_32x32x16_bf16 v[48:63], a[252:255], a[156:159], v[48:63]
	v_add_f32_e32 v158, v158, v154
	v_add_f32_e32 v159, v159, v155
	v_mfma_f32_32x32x16_bf16 v[32:47], a[252:255], a[188:191], v[32:47]
	s_add_i32 s7, s28, 0x80880
	v_add_f32_e32 v158, v158, v156
	v_add_f32_e32 v159, v159, v157
	v_add_f32_e32 v152, v152, v153
	s_waitcnt vmcnt(0) lgkmcnt(0)
	s_barrier
	v_mfma_f32_32x32x16_bf16 a[0:15], v[172:175], v[164:167], a[0:15]
	v_mov_b32_e32 v153, v152
	v_mfma_f32_32x32x16_bf16 a[16:31], v[172:175], v[196:199], a[16:31]
	s_nop 1
	v_permlane32_swap_b32_e32 v152, v153
	v_add_f32_e32 v152, v152, v153
	v_mfma_f32_32x32x16_bf16 a[32:47], v[180:183], v[164:167], a[32:47]
	v_add_f32_e32 v153, v219, v152
	v_add_f32_e32 v152, v158, v159
	v_mov_b32_e32 v158, v152
	v_mfma_f32_32x32x16_bf16 a[48:63], v[180:183], v[196:199], a[48:63]
	s_nop 1
	v_permlane32_swap_b32_e32 v152, v158
	v_add_f32_e32 v152, v152, v158
	v_mfma_f32_32x32x16_bf16 a[64:79], v[184:187], v[164:167], a[64:79]
	v_add_f32_e32 v152, v218, v152
	v_mfma_f32_32x32x16_bf16 a[80:95], v[184:187], v[196:199], a[80:95]
	v_mfma_f32_32x32x16_bf16 a[96:111], v[192:195], v[164:167], a[96:111]
	v_mfma_f32_32x32x16_bf16 a[112:127], v[192:195], v[196:199], a[112:127]
	v_mfma_f32_32x32x16_bf16 a[0:15], v[188:191], v[160:163], a[0:15]
	v_max3_f32 v158, v112, v113, v48
	v_max3_f32 v159, v114, v115, v49
	v_max3_f32 v158, v158, v50, v51
	v_mfma_f32_32x32x16_bf16 a[16:31], v[188:191], v[148:151], a[16:31]
	v_max3_f32 v158, v158, v116, v117
	v_max3_f32 v159, v159, v118, v119
	v_max3_f32 v158, v158, v52, v53
	v_max3_f32 v159, v159, v54, v55
	v_mfma_f32_32x32x16_bf16 a[32:47], v[176:179], v[160:163], a[32:47]
	v_max3_f32 v158, v158, v120, v121
	v_max3_f32 v159, v159, v122, v123
	v_max3_f32 v158, v158, v56, v57
	v_max3_f32 v159, v159, v58, v59
	v_mfma_f32_32x32x16_bf16 a[48:63], v[176:179], v[148:151], a[48:63]
	v_max3_f32 v158, v158, v124, v125
	v_max3_f32 v159, v159, v126, v127
	v_max3_f32 v158, v158, v60, v61
	v_max3_f32 v159, v159, v62, v63
	v_mfma_f32_32x32x16_bf16 a[64:79], v[168:171], v[160:163], a[64:79]
	v_max3_f32 v164, v96, v97, v32
	v_max3_f32 v165, v98, v99, v33
	v_max3_f32 v164, v164, v34, v35
	v_mfma_f32_32x32x16_bf16 a[80:95], v[168:171], v[148:151], a[80:95]
	v_max3_f32 v164, v164, v100, v101
	v_max3_f32 v165, v165, v102, v103
	v_max3_f32 v164, v164, v36, v37
	v_max3_f32 v165, v165, v38, v39
	v_mfma_f32_32x32x16_bf16 a[96:111], v[144:147], v[160:163], a[96:111]
	v_max3_f32 v160, v164, v104, v105
	v_max3_f32 v161, v165, v106, v107
	v_max3_f32 v160, v160, v40, v41
	v_max3_f32 v161, v161, v42, v43
	v_mfma_f32_32x32x16_bf16 a[112:127], v[144:147], v[148:151], a[112:127]
	v_max3_f32 v145, v161, v110, v111
	v_max3_f32 v144, v160, v108, v109
	v_max3_f32 v146, v144, v44, v45
	v_max3_f32 v145, v145, v46, v47
	v_mfma_f32_32x32x16_bf16 a[0:15], v[140:143], v[72:75], a[0:15]
	v_max_f32_e32 v144, v158, v159
	v_mov_b32_e32 v147, v144
	s_nop 1
	v_permlane32_swap_b32_e32 v144, v147
	v_max_f32_e32 v144, v144, v147
	v_mfma_f32_32x32x16_bf16 a[16:31], v[140:143], v[136:139], a[16:31]
	v_max_f32_e32 v140, v146, v145
	v_mov_b32_e32 v141, v140
	s_nop 1
	v_permlane32_swap_b32_e32 v140, v141
	v_max_f32_e32 v140, v140, v141
	v_max_f32_e32 v141, v144, v144
	v_max_f32_e32 v142, v140, v140
	v_max_f32_e32 v141, v141, v142
	s_mov_b32 s0, 0x41000000
	v_mfma_f32_32x32x16_bf16 a[32:47], v[66:69], v[72:75], a[32:47]
	v_cmp_lt_f32_e32 vcc, s0, v141
	s_cmp_lg_u64 vcc, 0
	s_cselect_b64 s[0:1], -1, 0
	s_cbranch_vccnz .LBB0_45
